# stack: two-row modulate0 loop, counted waits in NAT K/V prefetch, no redundant store drains in MoE scatter epilogue, 2208 conversion items moved from queue to scan phase
# speedup vs baseline: 1.0017x; 1.0017x over previous
.LBB0_620:
	s_and_b64 vcc, exec, s[4:5]
	s_cbranch_vccz .LBB0_760
	s_cmpk_lg_i32 s94, 0x100
	s_memrealtime s[4:5]
	s_cbranch_scc1 .LBB0_760
	v_readlane_b32 s2, v255, 25
	s_addk_i32 s2, 0xfc00
	s_cmp_gt_i32 s2, 0x895f
	v_readlane_b32 s3, v255, 26
	s_cbranch_scc1 .LBB0_760
	s_add_u32 s89, s84, 0x14b00000
	v_writelane_b32 v255, s95, 30
	s_addc_u32 s2, s85, 0
	v_writelane_b32 v255, s2, 38
	s_mul_i32 s2, s91, 0x2400
	s_waitcnt lgkmcnt(0)
	s_movk_i32 s4, 0x90
	s_waitcnt vmcnt(0)
	v_lshrrev_b32_e32 v14, 3, v1
	v_and_b32_e32 v3, 7, v0
	v_mov_b32_e32 v4, 0x480
	s_add_i32 s2, s2, 0
	v_lshlrev_b32_e32 v2, 4, v3
	v_lshlrev_b32_e32 v10, 3, v3
	v_mov_b32_e32 v3, 0
	v_mad_u32_u24 v18, v14, s4, v4
	v_mov_b32_e32 v4, 0x900
	v_mad_u32_u24 v20, v14, s4, v4
	s_add_u32 s3, s84, 0x4b00000
	v_lshl_add_u64 v[8:9], s[84:85], 0, v[2:3]
	s_mov_b64 s[4:5], 0x4300000
	v_writelane_b32 v255, s3, 33
	s_addc_u32 s3, s85, 0
	v_lshl_add_u64 v[4:5], v[8:9], 0, s[4:5]
	s_mov_b64 s[4:5], 0x2b00000
	v_writelane_b32 v255, s3, 27
	v_lshl_add_u64 v[6:7], v[8:9], 0, s[4:5]
	s_mov_b64 s[4:5], 0x2300000
	v_lshl_add_u64 v[8:9], v[8:9], 0, s[4:5]
	v_readlane_b32 s4, v255, 25
	v_readlane_b32 s5, v255, 26
	s_mov_b32 s6, s4
	s_add_i32 s12, s4, 0x3b40
	s_lshl_b32 s5, s91, 6
	s_lshl_b32 s4, s90, 9
	v_writelane_b32 v255, s91, 29
	s_mov_b32 s3, s5
	s_add_i32 s5, s4, s5
	v_mul_u32_u24_e32 v11, 0x90, v1
	v_add_u32_e32 v15, s2, v2
	v_writelane_b32 v255, s5, 31
	v_or_b32_e32 v2, s4, v1
	v_mul_u32_u24_e32 v16, 0x90, v14
	v_or_b32_e32 v17, 8, v14
	v_or_b32_e32 v19, 16, v14
	v_or_b32_e32 v21, 24, v14
	v_or_b32_e32 v22, 32, v14
	v_or_b32_e32 v23, 40, v14
	v_or_b32_e32 v24, 48, v14
	v_or_b32_e32 v25, 56, v14
	v_or_b32_e32 v26, 0xfffb0038, v14
	s_add_i32 s14, s6, 0xffffec00
	v_or_b32_e32 v27, 0xfffb0030, v14
	v_or_b32_e32 v28, 0xfffb0028, v14
	v_or_b32_e32 v29, 0xfffb0020, v14
	v_or_b32_e32 v30, 0xfffb0018, v14
	v_or_b32_e32 v31, 0xfffb0010, v14
	v_or_b32_e32 v32, 0xfffb0008, v14
	v_or_b32_e32 v33, 0xfffb0000, v14
	v_or_b32_e32 v34, 0xfffb0000, v1
	v_or_b32_e32 v35, 0xfffe0038, v14
	s_add_i32 s16, s6, 0xf800
	v_or_b32_e32 v36, 0xfffe0030, v14
	v_or_b32_e32 v37, 0xfffe0028, v14
	v_or_b32_e32 v38, 0xfffe0020, v14
	v_or_b32_e32 v39, 0xfffe0018, v14
	v_or_b32_e32 v40, 0xfffe0010, v14
	v_or_b32_e32 v41, 0xfffe0008, v14
	v_or_b32_e32 v42, 0xfffe0000, v14
	v_or_b32_e32 v43, 0xfffe0000, v1
	v_or_b32_e32 v44, s4, v14
	v_add_u32_e32 v45, 0xffff0000, v2
	s_movk_i32 s17, 0x800
	s_movk_i32 s18, 0x2000
	s_movk_i32 s19, 0x6000
	s_movk_i32 s20, 0x4000
	s_mov_b32 s21, 0xa000
	s_mov_b32 s22, 0x8000
	s_mov_b32 s23, 0xe000
	s_mov_b32 s24, 0xc000
	s_mov_b32 s25, 0x12000
	s_mov_b32 s26, 0x10000
	s_mov_b32 s27, 0x16000
	s_mov_b32 s28, 0x14000
	s_mov_b32 s29, 0x1a000
	s_mov_b32 s30, 0x18000
	s_mov_b32 s31, 0x1e000
	s_mov_b32 s34, 0x1c000
	s_mov_b32 s35, 0x22000
	s_mov_b32 s95, 0x20000
	s_mov_b32 s96, 0x26000
	s_mov_b32 s97, 0x24000
	s_mov_b32 s10, 0x2a000
	s_mov_b32 s13, 0x28000
	s_mov_b32 s8, 0x2e000
	s_mov_b32 s9, 0x2c000
	s_mov_b32 s54, 0x32000
	s_mov_b32 s57, 0x30000
	s_mov_b32 s53, 0x36000
	s_mov_b32 s58, 0x34000
	s_mov_b32 s59, 0x3a000
	s_mov_b32 s76, 0x38000
	s_mov_b32 s77, 0x3e000
	s_mov_b32 s52, 0x3c000
	s_mov_b32 s88, 0x42000
	s_mov_b32 s91, 0x60000
	s_mov_b32 s93, 0x66000
	s_mov_b32 s11, 0x6c000
	s_mov_b32 s15, 0x72000
	s_mov_b32 s55, 0x78000
	s_mov_b32 s56, 0x7e000
	v_add_u32_e32 v46, s2, v11
	s_movk_i32 s70, 0x400
	s_movk_i32 s71, 0x1800
	v_lshlrev_b32_e32 v2, 1, v10
	s_mov_b32 s74, 0
	s_mov_b32 s5, 0
	v_writelane_b32 v255, s89, 35
	s_branch .LBB0_626

.LBB0_625:
	s_addk_i32 s12, 0x400
	s_add_i32 s74, s74, 0x10000
	s_addk_i32 s14, 0x400
	s_addk_i32 s16, 0x400
	v_add_u32_e32 v44, 0x10000, v44
	s_cmp_gt_i32 s75, 0x855f
	v_add_u32_e32 v45, 0x10000, v45
	s_cbranch_scc1 .LBB0_759
.LBB0_626:
	s_add_i32 s75, s12, 0xffffc0c0
	s_cmpk_gt_i32 s75, 0x13ff
	s_mov_b64 s[6:7], -1
	s_cbranch_scc0 .LBB0_702
	s_cmpk_gt_u32 s75, 0x73ff
	s_cbranch_scc0 .LBB0_645
	s_add_i32 s98, s12, 0xfffff760
	s_bfe_u32 s2, s98, 0x50009
	s_and_b32 s33, s98, 0x1ff
	s_lshl_b32 s4, s2, 23
	s_add_u32 s47, s64, s4
	s_addc_u32 s79, s65, 0
	s_lshl_b32 s2, s2, 22
	s_add_u32 s4, s89, s2
	v_readlane_b32 s2, v255, 38
	s_addc_u32 s6, s2, 0
	s_bfe_u32 s7, s98, 0x40005
	s_lshl_b32 s2, s7, 11
	s_lshl_b32 s33, s33, 6
	s_sub_i32 s2, s33, s2
	v_or_b32_e32 v10, s2, v1
	s_lshl_b32 s33, s7, 19
	v_cmp_gt_i32_e32 vcc, s17, v10
	s_add_u32 s78, s47, s33
	s_addc_u32 s79, s79, 0
	v_cndmask_b32_e32 v10, 0, v10, vcc
	v_ashrrev_i32_e32 v11, 31, v10
	v_lshl_add_u64 v[10:11], v[10:11], 2, s[78:79]
	v_add_co_u32_e32 v12, vcc, s18, v10
	s_mov_b32 s33, 0x40000
	s_nop 0
	v_addc_co_u32_e32 v13, vcc, 0, v11, vcc
	v_add_co_u32_e32 v48, vcc, s19, v10
	global_load_dword v12, v[12:13], off nt
	s_nop 0
	global_load_dword v13, v[10:11], off nt
	v_addc_co_u32_e32 v49, vcc, 0, v11, vcc
	global_load_dword v47, v[48:49], off nt
	v_add_co_u32_e32 v48, vcc, s20, v10
	s_lshl_b32 s7, s7, 7
	s_nop 0
	v_addc_co_u32_e32 v49, vcc, 0, v11, vcc
	v_add_co_u32_e32 v50, vcc, s21, v10
	global_load_dword v48, v[48:49], off nt
	s_nop 0
	v_addc_co_u32_e32 v51, vcc, 0, v11, vcc
	global_load_dword v49, v[50:51], off nt
	v_add_co_u32_e32 v50, vcc, s22, v10
	s_add_u32 s78, s4, s7
	s_nop 0
	v_addc_co_u32_e32 v51, vcc, 0, v11, vcc
	v_add_co_u32_e32 v52, vcc, s23, v10
	global_load_dword v50, v[50:51], off nt
	s_nop 0
	v_addc_co_u32_e32 v53, vcc, 0, v11, vcc
	global_load_dword v51, v[52:53], off nt
	v_add_co_u32_e32 v52, vcc, s24, v10
	s_addc_u32 s79, s6, 0
	s_nop 0
	v_addc_co_u32_e32 v53, vcc, 0, v11, vcc
	v_add_co_u32_e32 v54, vcc, s25, v10
	global_load_dword v52, v[52:53], off nt
	s_nop 0
	v_addc_co_u32_e32 v55, vcc, 0, v11, vcc
	global_load_dword v53, v[54:55], off nt
	v_add_co_u32_e32 v54, vcc, s26, v10
	s_nop 1
	v_addc_co_u32_e32 v55, vcc, 0, v11, vcc
	v_add_co_u32_e32 v56, vcc, s27, v10
	global_load_dword v54, v[54:55], off nt
	s_nop 0
	v_addc_co_u32_e32 v57, vcc, 0, v11, vcc
	global_load_dword v55, v[56:57], off nt
	v_add_co_u32_e32 v56, vcc, s28, v10
	s_nop 1
	v_addc_co_u32_e32 v57, vcc, 0, v11, vcc
	v_add_co_u32_e32 v58, vcc, s29, v10
	global_load_dword v56, v[56:57], off nt
	s_nop 0
	v_addc_co_u32_e32 v59, vcc, 0, v11, vcc
	global_load_dword v57, v[58:59], off nt
	v_add_co_u32_e32 v58, vcc, s30, v10
	s_nop 1
	v_addc_co_u32_e32 v59, vcc, 0, v11, vcc
	v_add_co_u32_e32 v60, vcc, s31, v10
	global_load_dword v58, v[58:59], off nt
	s_nop 0
	v_addc_co_u32_e32 v61, vcc, 0, v11, vcc
	global_load_dword v59, v[60:61], off nt
	v_add_co_u32_e32 v60, vcc, s34, v10
	s_nop 1
	v_addc_co_u32_e32 v61, vcc, 0, v11, vcc
	v_add_co_u32_e32 v62, vcc, s35, v10
	global_load_dword v60, v[60:61], off nt
	s_nop 0
	v_addc_co_u32_e32 v63, vcc, 0, v11, vcc
	global_load_dword v61, v[62:63], off nt
	v_add_co_u32_e32 v62, vcc, s95, v10
	s_nop 1
	v_addc_co_u32_e32 v63, vcc, 0, v11, vcc
	v_add_co_u32_e32 v64, vcc, s96, v10
	global_load_dword v62, v[62:63], off nt
	s_nop 0
	v_addc_co_u32_e32 v65, vcc, 0, v11, vcc
	global_load_dword v63, v[64:65], off nt
	v_add_co_u32_e32 v64, vcc, s97, v10
	s_nop 1
	v_addc_co_u32_e32 v65, vcc, 0, v11, vcc
	v_add_co_u32_e32 v66, vcc, s10, v10
	global_load_dword v64, v[64:65], off nt
	s_nop 0
	v_addc_co_u32_e32 v67, vcc, 0, v11, vcc
	global_load_dword v65, v[66:67], off nt
	v_add_co_u32_e32 v66, vcc, s13, v10
	s_nop 1
	v_addc_co_u32_e32 v67, vcc, 0, v11, vcc
	v_add_co_u32_e32 v68, vcc, s8, v10
	global_load_dword v66, v[66:67], off nt
	s_nop 0
	v_addc_co_u32_e32 v69, vcc, 0, v11, vcc
	global_load_dword v67, v[68:69], off nt
	v_add_co_u32_e32 v68, vcc, s9, v10
	s_nop 1
	v_addc_co_u32_e32 v69, vcc, 0, v11, vcc
	v_add_co_u32_e32 v70, vcc, s54, v10
	global_load_dword v68, v[68:69], off nt
	s_nop 0
	v_addc_co_u32_e32 v71, vcc, 0, v11, vcc
	global_load_dword v69, v[70:71], off nt
	v_add_co_u32_e32 v70, vcc, s57, v10
	s_nop 1
	v_addc_co_u32_e32 v71, vcc, 0, v11, vcc
	v_add_co_u32_e32 v72, vcc, s53, v10
	global_load_dword v70, v[70:71], off nt
	s_nop 0
	v_addc_co_u32_e32 v73, vcc, 0, v11, vcc
	global_load_dword v71, v[72:73], off nt
	v_add_co_u32_e32 v72, vcc, s58, v10
	s_nop 1
	v_addc_co_u32_e32 v73, vcc, 0, v11, vcc
	v_add_co_u32_e32 v74, vcc, s59, v10
	global_load_dword v72, v[72:73], off nt
	s_nop 0
	v_addc_co_u32_e32 v75, vcc, 0, v11, vcc
	global_load_dword v73, v[74:75], off nt
	v_add_co_u32_e32 v74, vcc, s76, v10
	s_nop 1
	v_addc_co_u32_e32 v75, vcc, 0, v11, vcc
	v_add_co_u32_e32 v76, vcc, s77, v10
	global_load_dword v74, v[74:75], off nt
	s_nop 0
	v_addc_co_u32_e32 v77, vcc, 0, v11, vcc
	global_load_dword v75, v[76:77], off nt
	v_add_co_u32_e32 v76, vcc, s52, v10
	s_nop 1
	v_addc_co_u32_e32 v77, vcc, 0, v11, vcc
	global_load_dword v78, v[76:77], off nt
	v_add_co_u32_e32 v76, vcc, s88, v10
	s_nop 1
	v_addc_co_u32_e32 v77, vcc, 0, v11, vcc
	global_load_dword v79, v[76:77], off nt
	v_add_co_u32_e32 v76, vcc, s33, v10
	s_mov_b32 s33, 0x46000
	s_nop 0
	v_addc_co_u32_e32 v77, vcc, 0, v11, vcc
	global_load_dword v80, v[76:77], off nt
	v_add_co_u32_e32 v76, vcc, s33, v10
	s_mov_b32 s33, 0x44000
	s_nop 0
	v_addc_co_u32_e32 v77, vcc, 0, v11, vcc
	global_load_dword v81, v[76:77], off nt
	v_add_co_u32_e32 v76, vcc, s33, v10
	s_mov_b32 s33, 0x4a000
	s_nop 0
	v_addc_co_u32_e32 v77, vcc, 0, v11, vcc
	global_load_dword v82, v[76:77], off nt
	v_add_co_u32_e32 v76, vcc, s33, v10
	s_mov_b32 s33, 0x48000
	s_nop 0
	v_addc_co_u32_e32 v77, vcc, 0, v11, vcc
	global_load_dword v83, v[76:77], off nt
	v_add_co_u32_e32 v76, vcc, s33, v10
	s_mov_b32 s33, 0x4e000
	s_nop 0
	v_addc_co_u32_e32 v77, vcc, 0, v11, vcc
	global_load_dword v84, v[76:77], off nt
	v_add_co_u32_e32 v76, vcc, s33, v10
	s_mov_b32 s33, 0x4c000
	s_nop 0
	v_addc_co_u32_e32 v77, vcc, 0, v11, vcc
	global_load_dword v85, v[76:77], off nt
	v_add_co_u32_e32 v76, vcc, s33, v10
	s_mov_b32 s33, 0x52000
	s_nop 0
	v_addc_co_u32_e32 v77, vcc, 0, v11, vcc
	global_load_dword v86, v[76:77], off nt
	v_add_co_u32_e32 v76, vcc, s33, v10
	s_mov_b32 s33, 0x50000
	s_nop 0
	v_addc_co_u32_e32 v77, vcc, 0, v11, vcc
	global_load_dword v87, v[76:77], off nt
	v_add_co_u32_e32 v76, vcc, s33, v10
	s_mov_b32 s33, 0x56000
	s_nop 0
	v_addc_co_u32_e32 v77, vcc, 0, v11, vcc
	global_load_dword v88, v[76:77], off nt
	v_add_co_u32_e32 v76, vcc, s33, v10
	s_mov_b32 s33, 0x54000
	s_nop 0
	v_addc_co_u32_e32 v77, vcc, 0, v11, vcc
	global_load_dword v89, v[76:77], off nt
	v_add_co_u32_e32 v76, vcc, s33, v10
	s_mov_b32 s33, 0x5a000
	s_nop 0
	v_addc_co_u32_e32 v77, vcc, 0, v11, vcc
	global_load_dword v90, v[76:77], off nt
	v_add_co_u32_e32 v76, vcc, s33, v10
	s_mov_b32 s33, 0x58000
	s_nop 0
	v_addc_co_u32_e32 v77, vcc, 0, v11, vcc
	global_load_dword v91, v[76:77], off nt
	v_add_co_u32_e32 v76, vcc, s33, v10
	s_mov_b32 s33, 0x5e000
	s_nop 0
	v_addc_co_u32_e32 v77, vcc, 0, v11, vcc
	global_load_dword v92, v[76:77], off nt
	v_add_co_u32_e32 v76, vcc, s33, v10
	s_mov_b32 s33, 0x5c000
	s_nop 0
	v_addc_co_u32_e32 v77, vcc, 0, v11, vcc
	global_load_dword v93, v[76:77], off nt
	v_add_co_u32_e32 v76, vcc, s33, v10
	s_mov_b32 s33, 0x62000
	s_nop 0
	v_addc_co_u32_e32 v77, vcc, 0, v11, vcc
	global_load_dword v94, v[76:77], off nt
	v_add_co_u32_e32 v76, vcc, s33, v10
	s_mov_b32 s33, 0x64000
	s_nop 0
	v_addc_co_u32_e32 v77, vcc, 0, v11, vcc
	global_load_dword v95, v[76:77], off nt
	v_add_co_u32_e32 v76, vcc, s91, v10
	s_nop 1
	v_addc_co_u32_e32 v77, vcc, 0, v11, vcc
	global_load_dword v96, v[76:77], off nt
	v_add_co_u32_e32 v76, vcc, s93, v10
	s_nop 1
	v_addc_co_u32_e32 v77, vcc, 0, v11, vcc
	global_load_dword v97, v[76:77], off nt
	v_add_co_u32_e32 v76, vcc, s33, v10
	s_mov_b32 s33, 0x6a000
	s_nop 0
	v_addc_co_u32_e32 v77, vcc, 0, v11, vcc
	global_load_dword v98, v[76:77], off nt
	v_add_co_u32_e32 v76, vcc, s33, v10
	s_mov_b32 s33, 0x68000
	s_nop 0
	v_addc_co_u32_e32 v77, vcc, 0, v11, vcc
	global_load_dword v99, v[76:77], off nt
	v_add_co_u32_e32 v76, vcc, s33, v10
	s_mov_b32 s33, 0x6e000
	s_nop 0
	v_addc_co_u32_e32 v77, vcc, 0, v11, vcc
	global_load_dword v100, v[76:77], off nt
	v_add_co_u32_e32 v76, vcc, s33, v10
	s_mov_b32 s33, 0x70000
	s_nop 0
	v_addc_co_u32_e32 v77, vcc, 0, v11, vcc
	global_load_dword v101, v[76:77], off nt
	v_add_co_u32_e32 v76, vcc, s11, v10
	s_nop 1
	v_addc_co_u32_e32 v77, vcc, 0, v11, vcc
	global_load_dword v102, v[76:77], off nt
	v_add_co_u32_e32 v76, vcc, s15, v10
	s_nop 1
	v_addc_co_u32_e32 v77, vcc, 0, v11, vcc
	global_load_dword v103, v[76:77], off nt
	v_add_co_u32_e32 v76, vcc, s33, v10
	s_mov_b32 s33, 0x76000
	s_nop 0
	v_addc_co_u32_e32 v77, vcc, 0, v11, vcc
	global_load_dword v104, v[76:77], off nt
	v_add_co_u32_e32 v76, vcc, s33, v10
	s_mov_b32 s33, 0x74000
	s_nop 0
	v_addc_co_u32_e32 v77, vcc, 0, v11, vcc
	global_load_dword v105, v[76:77], off nt
	v_add_co_u32_e32 v76, vcc, s33, v10
	s_mov_b32 s33, 0x7a000
	s_nop 0
	v_addc_co_u32_e32 v77, vcc, 0, v11, vcc
	global_load_dword v106, v[76:77], off nt
	v_add_co_u32_e32 v76, vcc, s33, v10
	s_mov_b32 s33, 0x7c000
	s_nop 0
	v_addc_co_u32_e32 v77, vcc, 0, v11, vcc
	global_load_dword v107, v[76:77], off nt
	v_add_co_u32_e32 v76, vcc, s55, v10
	s_nop 1
	v_addc_co_u32_e32 v77, vcc, 0, v11, vcc
	global_load_dword v108, v[76:77], off nt
	v_add_co_u32_e32 v76, vcc, s56, v10
	s_nop 1
	v_addc_co_u32_e32 v77, vcc, 0, v11, vcc
	v_add_co_u32_e32 v10, vcc, s33, v10
	global_load_dword v76, v[76:77], off nt
	s_nop 0
	v_addc_co_u32_e32 v11, vcc, 0, v11, vcc
	global_load_dword v77, v[10:11], off nt
	s_waitcnt vmcnt(62)
	v_cvt_pk_bf16_f32 v10, v13, v12
	s_waitcnt vmcnt(60)
	v_cvt_pk_bf16_f32 v11, v48, v47
	s_waitcnt vmcnt(58)
	v_cvt_pk_bf16_f32 v12, v50, v49
	s_waitcnt vmcnt(56)
	v_cvt_pk_bf16_f32 v13, v52, v51
	ds_write_b128 v46, v[10:13]
	s_waitcnt vmcnt(54)
	v_cvt_pk_bf16_f32 v10, v54, v53
	s_waitcnt vmcnt(52)
	v_cvt_pk_bf16_f32 v11, v56, v55
	s_waitcnt vmcnt(50)
	v_cvt_pk_bf16_f32 v12, v58, v57
	s_waitcnt vmcnt(48)
	v_cvt_pk_bf16_f32 v13, v60, v59
	ds_write_b128 v46, v[10:13] offset:16
	s_waitcnt vmcnt(46)
	v_cvt_pk_bf16_f32 v10, v62, v61
	s_waitcnt vmcnt(44)
	v_cvt_pk_bf16_f32 v11, v64, v63
	s_waitcnt vmcnt(42)
	v_cvt_pk_bf16_f32 v12, v66, v65
	s_waitcnt vmcnt(40)
	v_cvt_pk_bf16_f32 v13, v68, v67
	ds_write_b128 v46, v[10:13] offset:32
	s_waitcnt vmcnt(38)
	v_cvt_pk_bf16_f32 v10, v70, v69
	s_waitcnt vmcnt(36)
	v_cvt_pk_bf16_f32 v11, v72, v71
	s_waitcnt vmcnt(34)
	v_cvt_pk_bf16_f32 v12, v74, v73
	s_waitcnt vmcnt(32)
	v_cvt_pk_bf16_f32 v13, v78, v75
	ds_write_b128 v46, v[10:13] offset:48
	s_waitcnt vmcnt(30)
	v_cvt_pk_bf16_f32 v10, v80, v79
	s_waitcnt vmcnt(28)
	v_cvt_pk_bf16_f32 v11, v82, v81
	s_waitcnt vmcnt(26)
	v_cvt_pk_bf16_f32 v12, v84, v83
	s_waitcnt vmcnt(24)
	v_cvt_pk_bf16_f32 v13, v86, v85
	ds_write_b128 v46, v[10:13] offset:64
	s_waitcnt vmcnt(22)
	v_cvt_pk_bf16_f32 v10, v88, v87
	s_waitcnt vmcnt(20)
	v_cvt_pk_bf16_f32 v11, v90, v89
	s_waitcnt vmcnt(18)
	v_cvt_pk_bf16_f32 v12, v92, v91
	s_waitcnt vmcnt(16)
	v_cvt_pk_bf16_f32 v13, v94, v93
	ds_write_b128 v46, v[10:13] offset:80
	s_waitcnt vmcnt(14)
	v_cvt_pk_bf16_f32 v10, v96, v95
	s_waitcnt vmcnt(12)
	v_cvt_pk_bf16_f32 v11, v98, v97
	s_waitcnt vmcnt(10)
	v_cvt_pk_bf16_f32 v12, v100, v99
	s_waitcnt vmcnt(8)
	v_cvt_pk_bf16_f32 v13, v102, v101
	ds_write_b128 v46, v[10:13] offset:96
	s_waitcnt vmcnt(6)
	v_cvt_pk_bf16_f32 v10, v104, v103
	s_waitcnt vmcnt(4)
	v_cvt_pk_bf16_f32 v11, v106, v105
	s_waitcnt vmcnt(2)
	v_cvt_pk_bf16_f32 v12, v108, v107
	s_waitcnt vmcnt(0)
	v_cvt_pk_bf16_f32 v13, v77, v76
	ds_write_b128 v46, v[10:13] offset:112
	s_waitcnt lgkmcnt(0)
	v_or_b32_e32 v12, s2, v14
	v_lshl_add_u64 v[10:11], s[78:79], 0, v[2:3]
	v_cmp_gt_i32_e32 vcc, s17, v12
	s_and_saveexec_b64 s[6:7], vcc
	s_cbranch_execz .LBB0_630
	v_add_u32_e32 v47, v15, v16
	ds_read_b128 v[48:51], v47
	v_ashrrev_i32_e32 v13, 31, v12
	v_lshlrev_b64 v[12:13], 11, v[12:13]
	v_lshl_add_u64 v[12:13], v[10:11], 0, v[12:13]
	s_waitcnt lgkmcnt(0)
	global_store_dwordx4 v[12:13], v[48:51], off nt

.LBB0_1078:
	s_or_b64 exec, exec, s[4:5]
	s_add_i32 s2, 0, 0x12000
	v_mov_b32_e32 v2, s2
	s_waitcnt lgkmcnt(0)
	s_barrier
	ds_read_b32 v2, v2
	s_movk_i32 s4, 0x1b5f
	s_mov_b32 s2, 0
	s_mov_b32 s8, 0x12000
	s_waitcnt lgkmcnt(0)
	v_cmp_lt_i32_e32 vcc, s4, v2
	v_readfirstlane_b32 s11, v2
	s_cbranch_vccnz .LBB0_1138
	s_add_u32 s9, s84, 0x14b00000
	s_mul_i32 s4, s91, 0x2400
	s_addc_u32 s10, s85, 0
	s_add_i32 s4, s4, 0
	v_and_b32_e32 v2, 7, v0
	v_mul_u32_u24_e32 v4, 0x90, v1
	v_lshrrev_b32_e32 v8, 3, v1
	v_lshl_add_u32 v9, v2, 4, s4
	v_lshlrev_b32_e32 v2, 3, v2
	v_mov_b32_e32 v3, 0
	v_mul_u32_u24_e32 v10, 0x90, v8
	v_or_b32_e32 v11, 8, v8
	v_or_b32_e32 v12, 16, v8
	v_or_b32_e32 v13, 24, v8
	v_or_b32_e32 v14, 32, v8
	v_or_b32_e32 v15, 40, v8
	v_or_b32_e32 v16, 48, v8
	v_or_b32_e32 v17, 56, v8
	s_add_i32 s11, s11, s91
	s_movk_i32 s12, 0x4000
	s_movk_i32 s13, 0x800
	s_movk_i32 s14, 0x2000
	s_movk_i32 s15, 0x6000
	s_mov_b32 s16, 0xa000
	s_mov_b32 s17, 0x8000
	s_mov_b32 s18, 0xe000
	s_mov_b32 s19, 0xc000
	s_mov_b32 s20, 0x10000
	s_mov_b32 s21, 0x16000
	s_mov_b32 s22, 0x14000
	s_mov_b32 s23, 0x1a000
	s_mov_b32 s24, 0x18000
	s_mov_b32 s25, 0x1e000
	s_mov_b32 s26, 0x1c000
	s_mov_b32 s27, 0x22000
	s_mov_b32 s28, 0x20000
	s_mov_b32 s29, 0x26000
	s_mov_b32 s30, 0x24000
	s_mov_b32 s31, 0x2a000
	s_mov_b32 s33, 0x28000
	s_mov_b32 s36, 0x2e000
	s_mov_b32 s37, 0x2c000
	s_mov_b32 s38, 0x32000
	s_mov_b32 s39, 0x30000
	s_mov_b32 s40, 0x36000
	s_mov_b32 s41, 0x34000
	s_mov_b32 s42, 0x3a000
	s_mov_b32 s43, 0x38000
	s_mov_b32 s44, 0x3e000
	s_mov_b32 s45, 0x3c000
	s_mov_b32 s47, 0x60000
	s_mov_b32 s48, 0x66000
	s_mov_b32 s49, 0x64000
	s_mov_b32 s50, 0x6a000
	s_mov_b32 s51, 0x68000
	s_mov_b32 s52, 0x6e000
	s_mov_b32 s53, 0x6c000
	s_mov_b32 s54, 0x72000
	s_mov_b32 s55, 0x70000
	s_mov_b32 s56, 0x76000
	s_mov_b32 s57, 0x74000
	s_mov_b32 s58, 0x7a000
	s_mov_b32 s59, 0x78000
	s_mov_b32 s68, 0x7e000
	s_mov_b32 s69, 0x7c000
	v_add_u32_e32 v18, s4, v4
	s_movk_i32 s70, 0x400
	s_mov_b32 s71, 0x3f000
	v_lshlrev_b32_e32 v2, 1, v2
	s_branch .LBB0_1082

.LBB0_1082:
	s_add_i32 s4, s11, s2
	s_cmpk_gt_i32 s4, 0x1b5f
	s_cbranch_scc1 .LBB0_1081
	s_add_i32 s5, s4, 0x2f40
	s_ashr_i32 s6, s5, 31
	s_lshr_b32 s6, s6, 19
	s_add_i32 s5, s5, s6
	s_and_b32 s5, s5, 0xffffe000
	s_add_i32 s6, s4, s5
	s_add_i32 s5, s6, 0x4f40
	s_ashr_i32 s4, s5, 31
	s_lshr_b32 s4, s4, 18
	s_add_i32 s4, s5, s4
	s_and_b32 s4, s4, 0xffffc000
	s_sub_i32 s7, s5, s4
	s_sext_i32_i16 s4, s7
	s_bfe_u32 s4, s4, 0x90016
	s_add_i32 s4, s7, s4
	s_sext_i32_i16 s72, s4
	s_ashr_i32 s4, s72, 9
	s_and_b32 s72, s72, 0xfffffe00
	s_sub_i32 s72, s7, s72
	s_add_i32 s6, s6, 0x8f3f
	s_cmpk_gt_u32 s6, 0x7ffe
	s_mov_b64 s[6:7], -1
	s_cbranch_scc0 .LBB0_1120
	s_and_b32 s5, s5, 0xffffc000
	s_cmpk_lg_i32 s5, 0x4000
	s_cbranch_scc0 .LBB0_1102
	s_ashr_i32 s5, s4, 31
	s_lshl_b64 s[6:7], s[4:5], 23
	s_add_u32 s75, s64, s6
	s_addc_u32 s78, s65, s7
	s_lshl_b64 s[6:7], s[4:5], 22
	s_add_u32 s73, s9, s6
	s_addc_u32 s74, s10, s7
	s_bfe_u32 s5, s72, 0x5001a
	s_add_i32 s5, s72, s5
	s_sext_i32_i16 s5, s5
	s_ashr_i32 s5, s5, 5
	s_lshl_b32 s6, s5, 6
	s_lshl_b32 s5, s5, 11
	s_lshl_b32 s7, s72, 6
	s_sub_i32 s5, s7, s5
	v_or_b32_e32 v4, s5, v1
	s_ashr_i32 s7, s6, 31
	s_lshl_b64 s[76:77], s[6:7], 13
	v_cmp_gt_i32_e32 vcc, s13, v4
	s_add_u32 s76, s75, s76
	s_addc_u32 s77, s78, s77
	v_cndmask_b32_e32 v4, 0, v4, vcc
	v_ashrrev_i32_e32 v5, 31, v4
	v_lshl_add_u64 v[4:5], v[4:5], 2, s[76:77]
	v_add_co_u32_e32 v6, vcc, s14, v4
	s_mov_b32 s75, 0x42000
	s_nop 0
	v_addc_co_u32_e32 v7, vcc, 0, v5, vcc
	global_load_dword v19, v[6:7], off nt
	global_load_dword v20, v[4:5], off nt
	v_add_co_u32_e32 v6, vcc, s15, v4
	s_lshl_b64 s[6:7], s[6:7], 1
	s_nop 0
	v_addc_co_u32_e32 v7, vcc, 0, v5, vcc
	global_load_dword v21, v[6:7], off nt
	v_add_co_u32_e32 v6, vcc, s12, v4
	s_add_u32 s6, s73, s6
	s_nop 0
	v_addc_co_u32_e32 v7, vcc, 0, v5, vcc
	global_load_dword v22, v[6:7], off nt
	v_add_co_u32_e32 v6, vcc, s16, v4
	s_addc_u32 s7, s74, s7
	s_nop 0
	v_addc_co_u32_e32 v7, vcc, 0, v5, vcc
	global_load_dword v23, v[6:7], off nt
	v_add_co_u32_e32 v6, vcc, s17, v4
	s_nop 1
	v_addc_co_u32_e32 v7, vcc, 0, v5, vcc
	global_load_dword v24, v[6:7], off nt
	v_add_co_u32_e32 v6, vcc, s18, v4
	s_nop 1
	v_addc_co_u32_e32 v7, vcc, 0, v5, vcc
	global_load_dword v25, v[6:7], off nt
	v_add_co_u32_e32 v6, vcc, s19, v4
	s_nop 1
	v_addc_co_u32_e32 v7, vcc, 0, v5, vcc
	global_load_dword v26, v[6:7], off nt
	v_add_co_u32_e32 v6, vcc, s8, v4
	s_nop 1
	v_addc_co_u32_e32 v7, vcc, 0, v5, vcc
	global_load_dword v27, v[6:7], off nt
	v_add_co_u32_e32 v6, vcc, s20, v4
	s_nop 1
	v_addc_co_u32_e32 v7, vcc, 0, v5, vcc
	global_load_dword v28, v[6:7], off nt
	v_add_co_u32_e32 v6, vcc, s21, v4
	s_nop 1
	v_addc_co_u32_e32 v7, vcc, 0, v5, vcc
	global_load_dword v29, v[6:7], off nt
	v_add_co_u32_e32 v6, vcc, s22, v4
	s_nop 1
	v_addc_co_u32_e32 v7, vcc, 0, v5, vcc
	global_load_dword v30, v[6:7], off nt
	v_add_co_u32_e32 v6, vcc, s23, v4
	s_nop 1
	v_addc_co_u32_e32 v7, vcc, 0, v5, vcc
	global_load_dword v31, v[6:7], off nt
	v_add_co_u32_e32 v6, vcc, s24, v4
	s_nop 1
	v_addc_co_u32_e32 v7, vcc, 0, v5, vcc
	global_load_dword v32, v[6:7], off nt
	v_add_co_u32_e32 v6, vcc, s25, v4
	s_nop 1
	v_addc_co_u32_e32 v7, vcc, 0, v5, vcc
	global_load_dword v33, v[6:7], off nt
	v_add_co_u32_e32 v6, vcc, s26, v4
	s_nop 1
	v_addc_co_u32_e32 v7, vcc, 0, v5, vcc
	global_load_dword v34, v[6:7], off nt
	v_add_co_u32_e32 v6, vcc, s27, v4
	s_nop 1
	v_addc_co_u32_e32 v7, vcc, 0, v5, vcc
	global_load_dword v35, v[6:7], off nt
	v_add_co_u32_e32 v6, vcc, s28, v4
	s_nop 1
	v_addc_co_u32_e32 v7, vcc, 0, v5, vcc
	global_load_dword v36, v[6:7], off nt
	v_add_co_u32_e32 v6, vcc, s29, v4
	s_nop 1
	v_addc_co_u32_e32 v7, vcc, 0, v5, vcc
	global_load_dword v37, v[6:7], off nt
	v_add_co_u32_e32 v6, vcc, s30, v4
	s_nop 1
	v_addc_co_u32_e32 v7, vcc, 0, v5, vcc
	global_load_dword v38, v[6:7], off nt
	v_add_co_u32_e32 v6, vcc, s31, v4
	s_nop 1
	v_addc_co_u32_e32 v7, vcc, 0, v5, vcc
	global_load_dword v39, v[6:7], off nt
	v_add_co_u32_e32 v6, vcc, s33, v4
	s_nop 1
	v_addc_co_u32_e32 v7, vcc, 0, v5, vcc
	global_load_dword v40, v[6:7], off nt
	v_add_co_u32_e32 v6, vcc, s36, v4
	s_nop 1
	v_addc_co_u32_e32 v7, vcc, 0, v5, vcc
	global_load_dword v41, v[6:7], off nt
	v_add_co_u32_e32 v6, vcc, s37, v4
	s_nop 1
	v_addc_co_u32_e32 v7, vcc, 0, v5, vcc
	global_load_dword v42, v[6:7], off nt
	v_add_co_u32_e32 v6, vcc, s38, v4
	s_nop 1
	v_addc_co_u32_e32 v7, vcc, 0, v5, vcc
	global_load_dword v43, v[6:7], off nt
	v_add_co_u32_e32 v6, vcc, s39, v4
	s_nop 1
	v_addc_co_u32_e32 v7, vcc, 0, v5, vcc
	global_load_dword v44, v[6:7], off nt
	v_add_co_u32_e32 v6, vcc, s40, v4
	s_nop 1
	v_addc_co_u32_e32 v7, vcc, 0, v5, vcc
	global_load_dword v45, v[6:7], off nt
	v_add_co_u32_e32 v6, vcc, s41, v4
	s_nop 1
	v_addc_co_u32_e32 v7, vcc, 0, v5, vcc
	global_load_dword v46, v[6:7], off nt
	v_add_co_u32_e32 v6, vcc, s42, v4
	s_nop 1
	v_addc_co_u32_e32 v7, vcc, 0, v5, vcc
	global_load_dword v47, v[6:7], off nt
	v_add_co_u32_e32 v6, vcc, s43, v4
	s_nop 1
	v_addc_co_u32_e32 v7, vcc, 0, v5, vcc
	global_load_dword v48, v[6:7], off nt
	v_add_co_u32_e32 v6, vcc, s44, v4
	s_nop 1
	v_addc_co_u32_e32 v7, vcc, 0, v5, vcc
	global_load_dword v49, v[6:7], off nt
	v_add_co_u32_e32 v6, vcc, s45, v4
	s_nop 1
	v_addc_co_u32_e32 v7, vcc, 0, v5, vcc
	global_load_dword v50, v[6:7], off nt
	v_add_co_u32_e32 v6, vcc, s75, v4
	s_mov_b32 s75, 0x40000
	s_nop 0
	v_addc_co_u32_e32 v7, vcc, 0, v5, vcc
	global_load_dword v51, v[6:7], off nt
	v_add_co_u32_e32 v6, vcc, s75, v4
	s_mov_b32 s75, 0x46000
	s_nop 0
	v_addc_co_u32_e32 v7, vcc, 0, v5, vcc
	global_load_dword v52, v[6:7], off nt
	v_add_co_u32_e32 v6, vcc, s75, v4
	s_mov_b32 s75, 0x44000
	s_nop 0
	v_addc_co_u32_e32 v7, vcc, 0, v5, vcc
	global_load_dword v53, v[6:7], off nt
	v_add_co_u32_e32 v6, vcc, s75, v4
	s_mov_b32 s75, 0x4a000
	s_nop 0
	v_addc_co_u32_e32 v7, vcc, 0, v5, vcc
	global_load_dword v54, v[6:7], off nt
	v_add_co_u32_e32 v6, vcc, s75, v4
	s_mov_b32 s75, 0x48000
	s_nop 0
	v_addc_co_u32_e32 v7, vcc, 0, v5, vcc
	global_load_dword v55, v[6:7], off nt
	v_add_co_u32_e32 v6, vcc, s75, v4
	s_mov_b32 s75, 0x4e000
	s_nop 0
	v_addc_co_u32_e32 v7, vcc, 0, v5, vcc
	global_load_dword v56, v[6:7], off nt
	v_add_co_u32_e32 v6, vcc, s75, v4
	s_mov_b32 s75, 0x4c000
	s_nop 0
	v_addc_co_u32_e32 v7, vcc, 0, v5, vcc
	global_load_dword v57, v[6:7], off nt
	v_add_co_u32_e32 v6, vcc, s75, v4
	s_mov_b32 s75, 0x52000
	s_nop 0
	v_addc_co_u32_e32 v7, vcc, 0, v5, vcc
	global_load_dword v58, v[6:7], off nt
	v_add_co_u32_e32 v6, vcc, s75, v4
	s_mov_b32 s75, 0x50000
	s_nop 0
	v_addc_co_u32_e32 v7, vcc, 0, v5, vcc
	global_load_dword v59, v[6:7], off nt
	v_add_co_u32_e32 v6, vcc, s75, v4
	s_mov_b32 s75, 0x56000
	s_nop 0
	v_addc_co_u32_e32 v7, vcc, 0, v5, vcc
	global_load_dword v60, v[6:7], off nt
	v_add_co_u32_e32 v6, vcc, s75, v4
	s_mov_b32 s75, 0x54000
	s_nop 0
	v_addc_co_u32_e32 v7, vcc, 0, v5, vcc
	global_load_dword v61, v[6:7], off nt
	v_add_co_u32_e32 v6, vcc, s75, v4
	s_mov_b32 s75, 0x5a000
	s_nop 0
	v_addc_co_u32_e32 v7, vcc, 0, v5, vcc
	global_load_dword v62, v[6:7], off nt
	v_add_co_u32_e32 v6, vcc, s75, v4
	s_mov_b32 s75, 0x58000
	s_nop 0
	v_addc_co_u32_e32 v7, vcc, 0, v5, vcc
	global_load_dword v63, v[6:7], off nt
	v_add_co_u32_e32 v6, vcc, s75, v4
	s_mov_b32 s75, 0x5e000
	s_nop 0
	v_addc_co_u32_e32 v7, vcc, 0, v5, vcc
	global_load_dword v64, v[6:7], off nt
	v_add_co_u32_e32 v6, vcc, s75, v4
	s_mov_b32 s75, 0x5c000
	s_nop 0
	v_addc_co_u32_e32 v7, vcc, 0, v5, vcc
	global_load_dword v65, v[6:7], off nt
	v_add_co_u32_e32 v6, vcc, s75, v4
	s_mov_b32 s75, 0x62000
	s_nop 0
	v_addc_co_u32_e32 v7, vcc, 0, v5, vcc
	global_load_dword v66, v[6:7], off nt
	v_add_co_u32_e32 v6, vcc, s75, v4
	s_nop 1
	v_addc_co_u32_e32 v7, vcc, 0, v5, vcc
	global_load_dword v67, v[6:7], off nt
	v_add_co_u32_e32 v6, vcc, s47, v4
	s_nop 1
	v_addc_co_u32_e32 v7, vcc, 0, v5, vcc
	global_load_dword v68, v[6:7], off nt
	v_add_co_u32_e32 v6, vcc, s48, v4
	s_nop 1
	v_addc_co_u32_e32 v7, vcc, 0, v5, vcc
	global_load_dword v69, v[6:7], off nt
	v_add_co_u32_e32 v6, vcc, s49, v4
	s_nop 1
	v_addc_co_u32_e32 v7, vcc, 0, v5, vcc
	global_load_dword v70, v[6:7], off nt
	v_add_co_u32_e32 v6, vcc, s50, v4
	s_nop 1
	v_addc_co_u32_e32 v7, vcc, 0, v5, vcc
	global_load_dword v71, v[6:7], off nt
	v_add_co_u32_e32 v6, vcc, s51, v4
	s_nop 1
	v_addc_co_u32_e32 v7, vcc, 0, v5, vcc
	global_load_dword v72, v[6:7], off nt
	v_add_co_u32_e32 v6, vcc, s52, v4
	s_nop 1
	v_addc_co_u32_e32 v7, vcc, 0, v5, vcc
	global_load_dword v73, v[6:7], off nt
	v_add_co_u32_e32 v6, vcc, s53, v4
	s_nop 1
	v_addc_co_u32_e32 v7, vcc, 0, v5, vcc
	global_load_dword v74, v[6:7], off nt
	v_add_co_u32_e32 v6, vcc, s54, v4
	s_nop 1
	v_addc_co_u32_e32 v7, vcc, 0, v5, vcc
	global_load_dword v75, v[6:7], off nt
	v_add_co_u32_e32 v6, vcc, s55, v4
	s_nop 1
	v_addc_co_u32_e32 v7, vcc, 0, v5, vcc
	global_load_dword v76, v[6:7], off nt
	v_add_co_u32_e32 v6, vcc, s56, v4
	s_nop 1
	v_addc_co_u32_e32 v7, vcc, 0, v5, vcc
	global_load_dword v77, v[6:7], off nt
	v_add_co_u32_e32 v6, vcc, s57, v4
	s_nop 1
	v_addc_co_u32_e32 v7, vcc, 0, v5, vcc
	global_load_dword v78, v[6:7], off nt
	v_add_co_u32_e32 v6, vcc, s58, v4
	s_nop 1
	v_addc_co_u32_e32 v7, vcc, 0, v5, vcc
	global_load_dword v79, v[6:7], off nt
	v_add_co_u32_e32 v6, vcc, s59, v4
	s_nop 1
	v_addc_co_u32_e32 v7, vcc, 0, v5, vcc
	global_load_dword v80, v[6:7], off nt
	v_add_co_u32_e32 v6, vcc, s68, v4
	s_nop 1
	v_addc_co_u32_e32 v7, vcc, 0, v5, vcc
	v_add_co_u32_e32 v4, vcc, s69, v4
	global_load_dword v81, v[6:7], off nt
	s_nop 0
	v_addc_co_u32_e32 v5, vcc, 0, v5, vcc
	global_load_dword v82, v[4:5], off nt
	s_waitcnt vmcnt(62)
	v_cvt_pk_bf16_f32 v4, v20, v19
	s_waitcnt vmcnt(60)
	v_cvt_pk_bf16_f32 v5, v22, v21
	s_waitcnt vmcnt(58)
	v_cvt_pk_bf16_f32 v6, v24, v23
	s_waitcnt vmcnt(56)
	v_cvt_pk_bf16_f32 v7, v26, v25
	ds_write_b128 v18, v[4:7]
	s_waitcnt vmcnt(54)
	v_cvt_pk_bf16_f32 v4, v28, v27
	s_waitcnt vmcnt(52)
	v_cvt_pk_bf16_f32 v5, v30, v29
	s_waitcnt vmcnt(50)
	v_cvt_pk_bf16_f32 v6, v32, v31
	s_waitcnt vmcnt(48)
	v_cvt_pk_bf16_f32 v7, v34, v33
	ds_write_b128 v18, v[4:7] offset:16
	s_waitcnt vmcnt(46)
	v_cvt_pk_bf16_f32 v4, v36, v35
	s_waitcnt vmcnt(44)
	v_cvt_pk_bf16_f32 v5, v38, v37
	s_waitcnt vmcnt(42)
	v_cvt_pk_bf16_f32 v6, v40, v39
	s_waitcnt vmcnt(40)
	v_cvt_pk_bf16_f32 v7, v42, v41
	ds_write_b128 v18, v[4:7] offset:32
	s_waitcnt vmcnt(38)
	v_cvt_pk_bf16_f32 v4, v44, v43
	s_waitcnt vmcnt(36)
	v_cvt_pk_bf16_f32 v5, v46, v45
	s_waitcnt vmcnt(34)
	v_cvt_pk_bf16_f32 v6, v48, v47
	s_waitcnt vmcnt(32)
	v_cvt_pk_bf16_f32 v7, v50, v49
	ds_write_b128 v18, v[4:7] offset:48
	s_waitcnt vmcnt(30)
	v_cvt_pk_bf16_f32 v4, v52, v51
	s_waitcnt vmcnt(28)
	v_cvt_pk_bf16_f32 v5, v54, v53
	s_waitcnt vmcnt(26)
	v_cvt_pk_bf16_f32 v6, v56, v55
	s_waitcnt vmcnt(24)
	v_cvt_pk_bf16_f32 v7, v58, v57
	ds_write_b128 v18, v[4:7] offset:64
	s_waitcnt vmcnt(22)
	v_cvt_pk_bf16_f32 v4, v60, v59
	s_waitcnt vmcnt(20)
	v_cvt_pk_bf16_f32 v5, v62, v61
	s_waitcnt vmcnt(18)
	v_cvt_pk_bf16_f32 v6, v64, v63
	s_waitcnt vmcnt(16)
	v_cvt_pk_bf16_f32 v7, v66, v65
	ds_write_b128 v18, v[4:7] offset:80
	s_waitcnt vmcnt(14)
	v_cvt_pk_bf16_f32 v4, v68, v67
	s_waitcnt vmcnt(12)
	v_cvt_pk_bf16_f32 v5, v70, v69
	s_waitcnt vmcnt(10)
	v_cvt_pk_bf16_f32 v6, v72, v71
	s_waitcnt vmcnt(8)
	v_cvt_pk_bf16_f32 v7, v74, v73
	ds_write_b128 v18, v[4:7] offset:96
	s_waitcnt vmcnt(6)
	v_cvt_pk_bf16_f32 v4, v76, v75
	s_waitcnt vmcnt(4)
	v_cvt_pk_bf16_f32 v5, v78, v77
	s_waitcnt vmcnt(2)
	v_cvt_pk_bf16_f32 v6, v80, v79
	s_waitcnt vmcnt(0)
	v_cvt_pk_bf16_f32 v7, v82, v81
	ds_write_b128 v18, v[4:7] offset:112
	s_waitcnt lgkmcnt(0)
	v_or_b32_e32 v6, s5, v8
	v_lshl_add_u64 v[4:5], s[6:7], 0, v[2:3]
	v_cmp_gt_i32_e32 vcc, s13, v6
	s_and_saveexec_b64 s[6:7], vcc
	s_cbranch_execz .LBB0_1087
	v_add_u32_e32 v7, v9, v10
	ds_read_b128 v[20:23], v7
	v_ashrrev_i32_e32 v7, 31, v6
	v_lshlrev_b64 v[6:7], 11, v[6:7]
	v_lshl_add_u64 v[6:7], v[4:5], 0, v[6:7]
	s_waitcnt lgkmcnt(0)
	global_store_dwordx4 v[6:7], v[20:23], off nt

.LBB0_1218:
	s_or_b64 exec, exec, s[6:7]
	s_nop 0
	v_add_u32_e32 v114, v165, v171
	v_cmp_lt_i32_e32 vcc, v114, v139
	s_and_saveexec_b64 s[6:7], vcc
	s_cbranch_execz .LBB0_1220
	s_nop 0
	v_ashrrev_i32_e32 v159, 31, v158
	v_lshlrev_b64 v[114:115], 12, v[158:159]
	v_lshl_add_u64 v[114:115], s[18:19], 0, v[114:115]
	v_lshl_add_u64 v[114:115], v[146:147], 1, v[114:115]
	v_pk_mul_f32 v[112:113], v[112:113], v[142:143] op_sel_hi:[1,0]
	v_pk_mul_f32 v[110:111], v[110:111], v[142:143] op_sel_hi:[1,0]
	v_pk_mul_f32 v[116:117], v[108:109], v[142:143] op_sel_hi:[1,0]
	v_pk_mul_f32 v[108:109], v[106:107], v[142:143] op_sel_hi:[1,0]
	v_cvt_pk_bf16_f32 v106, v110, v111
	v_cvt_pk_bf16_f32 v107, v112, v113
	v_pk_mul_f32 v[104:105], v[104:105], v[142:143] op_sel_hi:[1,0]
	v_cvt_pk_bf16_f32 v108, v108, v109
	v_cvt_pk_bf16_f32 v109, v116, v117
	global_store_dwordx4 v[114:115], v[106:109], off
	v_pk_mul_f32 v[102:103], v[102:103], v[142:143] op_sel_hi:[1,0]
	s_nop 0
	v_pk_mul_f32 v[106:107], v[100:101], v[142:143] op_sel_hi:[1,0]
	v_pk_mul_f32 v[100:101], v[98:99], v[142:143] op_sel_hi:[1,0]
	v_cvt_pk_bf16_f32 v98, v102, v103
	v_cvt_pk_bf16_f32 v99, v104, v105
	s_nop 0
	v_cvt_pk_bf16_f32 v100, v100, v101
	v_cvt_pk_bf16_f32 v101, v106, v107
	global_store_dwordx4 v[114:115], v[98:101], off offset:256
.LBB0_1220:
	s_or_b64 exec, exec, s[6:7]
	s_nop 0
	v_add_u32_e32 v98, v166, v171
	v_cmp_lt_i32_e32 vcc, v98, v139
	s_and_saveexec_b64 s[6:7], vcc
	s_cbranch_execz .LBB0_1222
	s_nop 0
	v_ashrrev_i32_e32 v157, 31, v156
	v_lshlrev_b64 v[98:99], 12, v[156:157]
	v_lshl_add_u64 v[98:99], s[18:19], 0, v[98:99]
	v_lshl_add_u64 v[98:99], v[146:147], 1, v[98:99]
	v_pk_mul_f32 v[96:97], v[96:97], v[138:139] op_sel_hi:[1,0]
	v_pk_mul_f32 v[94:95], v[94:95], v[138:139] op_sel_hi:[1,0]
	v_pk_mul_f32 v[100:101], v[92:93], v[138:139] op_sel_hi:[1,0]
	v_pk_mul_f32 v[92:93], v[90:91], v[138:139] op_sel_hi:[1,0]
	v_cvt_pk_bf16_f32 v90, v94, v95
	v_cvt_pk_bf16_f32 v91, v96, v97
	v_pk_mul_f32 v[88:89], v[88:89], v[138:139] op_sel_hi:[1,0]
	v_cvt_pk_bf16_f32 v92, v92, v93
	v_cvt_pk_bf16_f32 v93, v100, v101
	global_store_dwordx4 v[98:99], v[90:93], off
	v_pk_mul_f32 v[86:87], v[86:87], v[138:139] op_sel_hi:[1,0]
	s_nop 0
	v_pk_mul_f32 v[90:91], v[84:85], v[138:139] op_sel_hi:[1,0]
	v_pk_mul_f32 v[84:85], v[82:83], v[138:139] op_sel_hi:[1,0]
	v_cvt_pk_bf16_f32 v82, v86, v87
	v_cvt_pk_bf16_f32 v83, v88, v89
	s_nop 0
	v_cvt_pk_bf16_f32 v84, v84, v85
	v_cvt_pk_bf16_f32 v85, v90, v91
	global_store_dwordx4 v[98:99], v[82:85], off offset:256
.LBB0_1222:
	s_or_b64 exec, exec, s[6:7]
	s_nop 0
	v_add_u32_e32 v82, v167, v171
	v_cmp_lt_i32_e32 vcc, v82, v139
	s_and_saveexec_b64 s[6:7], vcc
	s_cbranch_execz .LBB0_1224
	s_nop 0
	v_ashrrev_i32_e32 v155, 31, v154
	v_lshlrev_b64 v[82:83], 12, v[154:155]
	v_lshl_add_u64 v[82:83], s[18:19], 0, v[82:83]
	v_lshl_add_u64 v[82:83], v[146:147], 1, v[82:83]
	v_pk_mul_f32 v[80:81], v[80:81], v[136:137] op_sel_hi:[1,0]
	v_pk_mul_f32 v[78:79], v[78:79], v[136:137] op_sel_hi:[1,0]
	v_pk_mul_f32 v[84:85], v[76:77], v[136:137] op_sel_hi:[1,0]
	v_pk_mul_f32 v[76:77], v[74:75], v[136:137] op_sel_hi:[1,0]
	v_cvt_pk_bf16_f32 v74, v78, v79
	v_cvt_pk_bf16_f32 v75, v80, v81
	v_pk_mul_f32 v[72:73], v[72:73], v[136:137] op_sel_hi:[1,0]
	v_cvt_pk_bf16_f32 v76, v76, v77
	v_cvt_pk_bf16_f32 v77, v84, v85
	global_store_dwordx4 v[82:83], v[74:77], off
	v_pk_mul_f32 v[70:71], v[70:71], v[136:137] op_sel_hi:[1,0]
	s_nop 0
	v_pk_mul_f32 v[74:75], v[68:69], v[136:137] op_sel_hi:[1,0]
	v_pk_mul_f32 v[68:69], v[66:67], v[136:137] op_sel_hi:[1,0]
	v_cvt_pk_bf16_f32 v66, v70, v71
	v_cvt_pk_bf16_f32 v67, v72, v73
	s_nop 0
	v_cvt_pk_bf16_f32 v68, v68, v69
	v_cvt_pk_bf16_f32 v69, v74, v75
	global_store_dwordx4 v[82:83], v[66:69], off offset:256

.LBB0_1227:
	s_nop 0
	v_ashrrev_i32_e32 v73, 31, v72
	v_lshlrev_b64 v[26:27], 12, v[72:73]
	v_lshl_add_u64 v[26:27], s[18:19], 0, v[26:27]
	v_pk_mul_f32 v[28:29], v[12:13], v[70:71] op_sel_hi:[1,0]
	v_pk_mul_f32 v[12:13], v[10:11], v[70:71] op_sel_hi:[1,0]
	v_lshl_add_u64 v[26:27], v[146:147], 1, v[26:27]
	v_pk_mul_f32 v[16:17], v[16:17], v[70:71] op_sel_hi:[1,0]
	v_pk_mul_f32 v[14:15], v[14:15], v[70:71] op_sel_hi:[1,0]
	s_nop 0
	v_cvt_pk_bf16_f32 v10, v14, v15
	v_cvt_pk_bf16_f32 v11, v16, v17
	v_cvt_pk_bf16_f32 v12, v12, v13
	v_cvt_pk_bf16_f32 v13, v28, v29
	global_store_dwordx4 v[26:27], v[10:13], off
	v_pk_mul_f32 v[14:15], v[40:41], v[70:71] op_sel_hi:[1,0]
	v_pk_mul_f32 v[16:17], v[38:39], v[70:71] op_sel_hi:[1,0]
	v_pk_mul_f32 v[12:13], v[36:37], v[70:71] op_sel_hi:[1,0]
	v_pk_mul_f32 v[10:11], v[34:35], v[70:71] op_sel_hi:[1,0]
	s_nop 0
	v_cvt_pk_bf16_f32 v10, v10, v11
	v_cvt_pk_bf16_f32 v11, v12, v13
	v_cvt_pk_bf16_f32 v12, v16, v17
	v_cvt_pk_bf16_f32 v13, v14, v15
	global_store_dwordx4 v[26:27], v[10:13], off offset:256
	s_or_b64 exec, exec, s[6:7]
	v_cmp_lt_i32_e32 vcc, v67, v139
	s_and_saveexec_b64 s[6:7], vcc
	s_cbranch_execnz .LBB0_1232

.LBB0_1230:
	s_nop 0
	v_ashrrev_i32_e32 v77, 31, v76
	v_lshlrev_b64 v[50:51], 12, v[76:77]
	v_lshl_add_u64 v[50:51], s[18:19], 0, v[50:51]
	v_lshl_add_u64 v[50:51], v[146:147], 1, v[50:51]
	v_pk_mul_f32 v[48:49], v[48:49], v[74:75] op_sel_hi:[1,0]
	v_pk_mul_f32 v[46:47], v[46:47], v[74:75] op_sel_hi:[1,0]
	v_pk_mul_f32 v[52:53], v[44:45], v[74:75] op_sel_hi:[1,0]
	v_pk_mul_f32 v[44:45], v[42:43], v[74:75] op_sel_hi:[1,0]
	v_cvt_pk_bf16_f32 v42, v46, v47
	v_cvt_pk_bf16_f32 v43, v48, v49
	v_pk_mul_f32 v[32:33], v[32:33], v[74:75] op_sel_hi:[1,0]
	v_cvt_pk_bf16_f32 v44, v44, v45
	v_cvt_pk_bf16_f32 v45, v52, v53
	global_store_dwordx4 v[50:51], v[42:45], off
	v_pk_mul_f32 v[30:31], v[30:31], v[74:75] op_sel_hi:[1,0]
	s_nop 0
	v_pk_mul_f32 v[42:43], v[28:29], v[74:75] op_sel_hi:[1,0]
	v_pk_mul_f32 v[28:29], v[26:27], v[74:75] op_sel_hi:[1,0]
	v_cvt_pk_bf16_f32 v26, v30, v31
	v_cvt_pk_bf16_f32 v27, v32, v33
	s_nop 0
	v_cvt_pk_bf16_f32 v28, v28, v29
	v_cvt_pk_bf16_f32 v29, v42, v43
	global_store_dwordx4 v[50:51], v[26:29], off offset:256
	s_or_b64 exec, exec, s[6:7]
	v_cmp_lt_i32_e32 vcc, v69, v139
	s_and_saveexec_b64 s[6:7], vcc
	s_cbranch_execnz .LBB0_1227

.LBB0_1232:
	s_nop 0
	v_ashrrev_i32_e32 v69, 31, v68
	v_lshlrev_b64 v[10:11], 12, v[68:69]
	v_lshl_add_u64 v[10:11], s[18:19], 0, v[10:11]
	v_pk_mul_f32 v[12:13], v[4:5], v[66:67] op_sel_hi:[1,0]
	v_pk_mul_f32 v[4:5], v[2:3], v[66:67] op_sel_hi:[1,0]
	v_lshl_add_u64 v[10:11], v[146:147], 1, v[10:11]
	v_pk_mul_f32 v[8:9], v[8:9], v[66:67] op_sel_hi:[1,0]
	v_pk_mul_f32 v[6:7], v[6:7], v[66:67] op_sel_hi:[1,0]
	s_nop 0
	v_cvt_pk_bf16_f32 v2, v6, v7
	v_cvt_pk_bf16_f32 v3, v8, v9
	v_cvt_pk_bf16_f32 v4, v4, v5
	v_cvt_pk_bf16_f32 v5, v12, v13
	global_store_dwordx4 v[10:11], v[2:5], off
	v_pk_mul_f32 v[6:7], v[24:25], v[66:67] op_sel_hi:[1,0]
	v_pk_mul_f32 v[8:9], v[22:23], v[66:67] op_sel_hi:[1,0]
	v_pk_mul_f32 v[4:5], v[20:21], v[66:67] op_sel_hi:[1,0]
	v_pk_mul_f32 v[2:3], v[18:19], v[66:67] op_sel_hi:[1,0]
	s_nop 0
	v_cvt_pk_bf16_f32 v2, v2, v3
	v_cvt_pk_bf16_f32 v3, v4, v5
	v_cvt_pk_bf16_f32 v4, v8, v9
	v_cvt_pk_bf16_f32 v5, v6, v7
	global_store_dwordx4 v[10:11], v[2:5], off offset:256
	s_or_b64 exec, exec, s[6:7]
	s_and_b64 vcc, exec, s[4:5]
	s_mov_b64 s[4:5], -1
	s_cbranch_vccnz .LBB0_1207

.LBB0_1244:
	s_or_b64 exec, exec, s[6:7]
	s_waitcnt lgkmcnt(0)
	s_barrier
	ds_read_b32 v4, v18
	s_movk_i32 s6, 0x1b5f
	s_waitcnt lgkmcnt(0)
	v_cmp_lt_i32_e32 vcc, s6, v4
	v_readfirstlane_b32 s71, v4
	s_mov_b64 s[6:7], -1
	s_cbranch_vccnz .LBB0_1239
	s_add_i32 s71, s71, s91
	s_mov_b32 s8, 0
	s_mov_b64 s[6:7], 0
	s_branch .LBB0_1248

.LBB0_1248:
	s_add_i32 s8, s71, s8
	s_cmpk_gt_i32 s8, 0x1b5f
	s_cbranch_scc1 .LBB0_1247
	s_addk_i32 s8, 0x2f40
	s_ashr_i32 s9, s8, 31
	s_lshr_b32 s9, s9, 19
	s_add_i32 s9, s8, s9
	s_and_b32 s10, s9, 0xffffe000
	s_lshl_b32 s9, s9, 1
	s_sub_i32 s8, s8, s10
	s_and_b32 s9, s9, 0xffffc000
	s_add_i32 s10, s8, s9
	s_add_i32 s9, s10, 0x2000
	s_ashr_i32 s8, s9, 31
	s_lshr_b32 s8, s8, 18
	s_add_i32 s8, s9, s8
	s_and_b32 s8, s8, 0xffffc000
	s_sub_i32 s11, s9, s8
	s_sext_i32_i16 s8, s11
	s_bfe_u32 s8, s8, 0x90016
	s_add_i32 s8, s11, s8
	s_sext_i32_i16 s72, s8
	s_ashr_i32 s8, s72, 9
	s_and_b32 s72, s72, 0xfffffe00
	s_sub_i32 s72, s11, s72
	s_addk_i32 s10, 0x5fff
	s_cmpk_gt_u32 s10, 0x7ffe
	s_mov_b64 s[10:11], -1
	s_cbranch_scc0 .LBB0_1286
	s_and_b32 s9, s9, 0xffffc000
	s_cmpk_lg_i32 s9, 0x4000
	s_cbranch_scc0 .LBB0_1268
	s_ashr_i32 s9, s8, 31
	s_lshl_b64 s[10:11], s[8:9], 23
	s_add_u32 s75, s64, s10
	s_addc_u32 s78, s65, s11
	s_lshl_b64 s[10:11], s[8:9], 22
	s_add_u32 s73, s2, s10
	s_addc_u32 s74, s33, s11
	s_bfe_u32 s9, s72, 0x5001a
	s_add_i32 s9, s72, s9
	s_sext_i32_i16 s9, s9
	s_ashr_i32 s9, s9, 5
	s_lshl_b32 s10, s9, 6
	s_lshl_b32 s9, s9, 11
	s_lshl_b32 s11, s72, 6
	s_sub_i32 s9, s11, s9
	v_or_b32_e32 v4, s9, v1
	s_ashr_i32 s11, s10, 31
	s_lshl_b64 s[76:77], s[10:11], 13
	v_cmp_gt_i32_e32 vcc, s19, v4
	s_add_u32 s76, s75, s76
	s_addc_u32 s77, s78, s77
	v_cndmask_b32_e32 v4, 0, v4, vcc
	v_ashrrev_i32_e32 v5, 31, v4
	v_lshl_add_u64 v[4:5], v[4:5], 2, s[76:77]
	v_add_co_u32_e32 v6, vcc, s17, v4
	s_mov_b32 s75, 0x42000
	s_nop 0
	v_addc_co_u32_e32 v7, vcc, 0, v5, vcc
	global_load_dword v20, v[6:7], off nt
	global_load_dword v21, v[4:5], off nt
	v_add_co_u32_e32 v6, vcc, s20, v4
	s_lshl_b64 s[10:11], s[10:11], 1
	s_nop 0
	v_addc_co_u32_e32 v7, vcc, 0, v5, vcc
	global_load_dword v22, v[6:7], off nt
	v_add_co_u32_e32 v6, vcc, s18, v4
	s_add_u32 s10, s73, s10
	s_nop 0
	v_addc_co_u32_e32 v7, vcc, 0, v5, vcc
	global_load_dword v23, v[6:7], off nt
	v_add_co_u32_e32 v6, vcc, s21, v4
	s_addc_u32 s11, s74, s11
	s_nop 0
	v_addc_co_u32_e32 v7, vcc, 0, v5, vcc
	global_load_dword v24, v[6:7], off nt
	v_add_co_u32_e32 v6, vcc, s22, v4
	s_nop 1
	v_addc_co_u32_e32 v7, vcc, 0, v5, vcc
	global_load_dword v25, v[6:7], off nt
	v_add_co_u32_e32 v6, vcc, s23, v4
	s_nop 1
	v_addc_co_u32_e32 v7, vcc, 0, v5, vcc
	global_load_dword v26, v[6:7], off nt
	v_add_co_u32_e32 v6, vcc, s24, v4
	s_nop 1
	v_addc_co_u32_e32 v7, vcc, 0, v5, vcc
	global_load_dword v27, v[6:7], off nt
	v_add_co_u32_e32 v6, vcc, s15, v4
	s_nop 1
	v_addc_co_u32_e32 v7, vcc, 0, v5, vcc
	global_load_dword v28, v[6:7], off nt
	v_add_co_u32_e32 v6, vcc, s25, v4
	s_nop 1
	v_addc_co_u32_e32 v7, vcc, 0, v5, vcc
	global_load_dword v29, v[6:7], off nt
	v_add_co_u32_e32 v6, vcc, s26, v4
	s_nop 1
	v_addc_co_u32_e32 v7, vcc, 0, v5, vcc
	global_load_dword v30, v[6:7], off nt
	v_add_co_u32_e32 v6, vcc, s27, v4
	s_nop 1
	v_addc_co_u32_e32 v7, vcc, 0, v5, vcc
	global_load_dword v31, v[6:7], off nt
	v_add_co_u32_e32 v6, vcc, s28, v4
	s_nop 1
	v_addc_co_u32_e32 v7, vcc, 0, v5, vcc
	global_load_dword v32, v[6:7], off nt
	v_add_co_u32_e32 v6, vcc, s29, v4
	s_nop 1
	v_addc_co_u32_e32 v7, vcc, 0, v5, vcc
	global_load_dword v33, v[6:7], off nt
	v_add_co_u32_e32 v6, vcc, s30, v4
	s_nop 1
	v_addc_co_u32_e32 v7, vcc, 0, v5, vcc
	global_load_dword v34, v[6:7], off nt
	v_add_co_u32_e32 v6, vcc, s31, v4
	s_nop 1
	v_addc_co_u32_e32 v7, vcc, 0, v5, vcc
	global_load_dword v35, v[6:7], off nt
	v_add_co_u32_e32 v6, vcc, s34, v4
	s_nop 1
	v_addc_co_u32_e32 v7, vcc, 0, v5, vcc
	global_load_dword v36, v[6:7], off nt
	v_add_co_u32_e32 v6, vcc, s35, v4
	s_nop 1
	v_addc_co_u32_e32 v7, vcc, 0, v5, vcc
	global_load_dword v37, v[6:7], off nt
	v_add_co_u32_e32 v6, vcc, s36, v4
	s_nop 1
	v_addc_co_u32_e32 v7, vcc, 0, v5, vcc
	global_load_dword v38, v[6:7], off nt
	v_add_co_u32_e32 v6, vcc, s37, v4
	s_nop 1
	v_addc_co_u32_e32 v7, vcc, 0, v5, vcc
	global_load_dword v39, v[6:7], off nt
	v_add_co_u32_e32 v6, vcc, s38, v4
	s_nop 1
	v_addc_co_u32_e32 v7, vcc, 0, v5, vcc
	global_load_dword v40, v[6:7], off nt
	v_add_co_u32_e32 v6, vcc, s39, v4
	s_nop 1
	v_addc_co_u32_e32 v7, vcc, 0, v5, vcc
	global_load_dword v41, v[6:7], off nt
	v_add_co_u32_e32 v6, vcc, s40, v4
	s_nop 1
	v_addc_co_u32_e32 v7, vcc, 0, v5, vcc
	global_load_dword v42, v[6:7], off nt
	v_add_co_u32_e32 v6, vcc, s41, v4
	s_nop 1
	v_addc_co_u32_e32 v7, vcc, 0, v5, vcc
	global_load_dword v43, v[6:7], off nt
	v_add_co_u32_e32 v6, vcc, s42, v4
	s_nop 1
	v_addc_co_u32_e32 v7, vcc, 0, v5, vcc
	global_load_dword v44, v[6:7], off nt
	v_add_co_u32_e32 v6, vcc, s43, v4
	s_nop 1
	v_addc_co_u32_e32 v7, vcc, 0, v5, vcc
	global_load_dword v45, v[6:7], off nt
	v_add_co_u32_e32 v6, vcc, s44, v4
	s_nop 1
	v_addc_co_u32_e32 v7, vcc, 0, v5, vcc
	global_load_dword v46, v[6:7], off nt
	v_add_co_u32_e32 v6, vcc, s45, v4
	s_nop 1
	v_addc_co_u32_e32 v7, vcc, 0, v5, vcc
	global_load_dword v47, v[6:7], off nt
	v_add_co_u32_e32 v6, vcc, s47, v4
	s_nop 1
	v_addc_co_u32_e32 v7, vcc, 0, v5, vcc
	global_load_dword v48, v[6:7], off nt
	v_add_co_u32_e32 v6, vcc, s48, v4
	s_nop 1
	v_addc_co_u32_e32 v7, vcc, 0, v5, vcc
	global_load_dword v49, v[6:7], off nt
	v_add_co_u32_e32 v6, vcc, s49, v4
	s_nop 1
	v_addc_co_u32_e32 v7, vcc, 0, v5, vcc
	global_load_dword v50, v[6:7], off nt
	v_add_co_u32_e32 v6, vcc, s50, v4
	s_nop 1
	v_addc_co_u32_e32 v7, vcc, 0, v5, vcc
	global_load_dword v51, v[6:7], off nt
	v_add_co_u32_e32 v6, vcc, s75, v4
	s_mov_b32 s75, 0x40000
	s_nop 0
	v_addc_co_u32_e32 v7, vcc, 0, v5, vcc
	global_load_dword v52, v[6:7], off nt
	v_add_co_u32_e32 v6, vcc, s75, v4
	s_mov_b32 s75, 0x46000
	s_nop 0
	v_addc_co_u32_e32 v7, vcc, 0, v5, vcc
	global_load_dword v53, v[6:7], off nt
	v_add_co_u32_e32 v6, vcc, s75, v4
	s_mov_b32 s75, 0x44000
	s_nop 0
	v_addc_co_u32_e32 v7, vcc, 0, v5, vcc
	global_load_dword v54, v[6:7], off nt
	v_add_co_u32_e32 v6, vcc, s75, v4
	s_mov_b32 s75, 0x4a000
	s_nop 0
	v_addc_co_u32_e32 v7, vcc, 0, v5, vcc
	global_load_dword v55, v[6:7], off nt
	v_add_co_u32_e32 v6, vcc, s75, v4
	s_mov_b32 s75, 0x48000
	s_nop 0
	v_addc_co_u32_e32 v7, vcc, 0, v5, vcc
	global_load_dword v56, v[6:7], off nt
	v_add_co_u32_e32 v6, vcc, s75, v4
	s_mov_b32 s75, 0x4e000
	s_nop 0
	v_addc_co_u32_e32 v7, vcc, 0, v5, vcc
	global_load_dword v57, v[6:7], off nt
	v_add_co_u32_e32 v6, vcc, s75, v4
	s_mov_b32 s75, 0x4c000
	s_nop 0
	v_addc_co_u32_e32 v7, vcc, 0, v5, vcc
	global_load_dword v58, v[6:7], off nt
	v_add_co_u32_e32 v6, vcc, s75, v4
	s_mov_b32 s75, 0x52000
	s_nop 0
	v_addc_co_u32_e32 v7, vcc, 0, v5, vcc
	global_load_dword v59, v[6:7], off nt
	v_add_co_u32_e32 v6, vcc, s75, v4
	s_mov_b32 s75, 0x50000
	s_nop 0
	v_addc_co_u32_e32 v7, vcc, 0, v5, vcc
	global_load_dword v60, v[6:7], off nt
	v_add_co_u32_e32 v6, vcc, s75, v4
	s_mov_b32 s75, 0x56000
	s_nop 0
	v_addc_co_u32_e32 v7, vcc, 0, v5, vcc
	global_load_dword v61, v[6:7], off nt
	v_add_co_u32_e32 v6, vcc, s75, v4
	s_mov_b32 s75, 0x54000
	s_nop 0
	v_addc_co_u32_e32 v7, vcc, 0, v5, vcc
	global_load_dword v62, v[6:7], off nt
	v_add_co_u32_e32 v6, vcc, s75, v4
	s_mov_b32 s75, 0x5a000
	s_nop 0
	v_addc_co_u32_e32 v7, vcc, 0, v5, vcc
	global_load_dword v63, v[6:7], off nt
	v_add_co_u32_e32 v6, vcc, s75, v4
	s_mov_b32 s75, 0x58000
	s_nop 0
	v_addc_co_u32_e32 v7, vcc, 0, v5, vcc
	global_load_dword v64, v[6:7], off nt
	v_add_co_u32_e32 v6, vcc, s75, v4
	s_mov_b32 s75, 0x5e000
	s_nop 0
	v_addc_co_u32_e32 v7, vcc, 0, v5, vcc
	global_load_dword v65, v[6:7], off nt
	v_add_co_u32_e32 v6, vcc, s75, v4
	s_mov_b32 s75, 0x5c000
	s_nop 0
	v_addc_co_u32_e32 v7, vcc, 0, v5, vcc
	global_load_dword v66, v[6:7], off nt
	v_add_co_u32_e32 v6, vcc, s75, v4
	s_mov_b32 s75, 0x62000
	s_nop 0
	v_addc_co_u32_e32 v7, vcc, 0, v5, vcc
	global_load_dword v67, v[6:7], off nt
	v_add_co_u32_e32 v6, vcc, s75, v4
	s_mov_b32 s75, 0x60000
	s_nop 0
	v_addc_co_u32_e32 v7, vcc, 0, v5, vcc
	global_load_dword v68, v[6:7], off nt
	v_add_co_u32_e32 v6, vcc, s75, v4
	s_mov_b32 s75, 0x66000
	s_nop 0
	v_addc_co_u32_e32 v7, vcc, 0, v5, vcc
	global_load_dword v69, v[6:7], off nt
	v_add_co_u32_e32 v6, vcc, s75, v4
	s_mov_b32 s75, 0x64000
	s_nop 0
	v_addc_co_u32_e32 v7, vcc, 0, v5, vcc
	global_load_dword v70, v[6:7], off nt
	v_add_co_u32_e32 v6, vcc, s75, v4
	s_mov_b32 s75, 0x6a000
	s_nop 0
	v_addc_co_u32_e32 v7, vcc, 0, v5, vcc
	global_load_dword v71, v[6:7], off nt
	v_add_co_u32_e32 v6, vcc, s75, v4
	s_mov_b32 s75, 0x68000
	s_nop 0
	v_addc_co_u32_e32 v7, vcc, 0, v5, vcc
	global_load_dword v72, v[6:7], off nt
	v_add_co_u32_e32 v6, vcc, s75, v4
	s_nop 1
	v_addc_co_u32_e32 v7, vcc, 0, v5, vcc
	global_load_dword v73, v[6:7], off nt
	v_add_co_u32_e32 v6, vcc, s51, v4
	s_nop 1
	v_addc_co_u32_e32 v7, vcc, 0, v5, vcc
	global_load_dword v74, v[6:7], off nt
	v_add_co_u32_e32 v6, vcc, s52, v4
	s_nop 1
	v_addc_co_u32_e32 v7, vcc, 0, v5, vcc
	global_load_dword v75, v[6:7], off nt
	v_add_co_u32_e32 v6, vcc, s53, v4
	s_nop 1
	v_addc_co_u32_e32 v7, vcc, 0, v5, vcc
	global_load_dword v76, v[6:7], off nt
	v_add_co_u32_e32 v6, vcc, s54, v4
	s_nop 1
	v_addc_co_u32_e32 v7, vcc, 0, v5, vcc
	global_load_dword v77, v[6:7], off nt
	v_add_co_u32_e32 v6, vcc, s55, v4
	s_nop 1
	v_addc_co_u32_e32 v7, vcc, 0, v5, vcc
	global_load_dword v78, v[6:7], off nt
	v_add_co_u32_e32 v6, vcc, s56, v4
	s_nop 1
	v_addc_co_u32_e32 v7, vcc, 0, v5, vcc
	global_load_dword v79, v[6:7], off nt
	v_add_co_u32_e32 v6, vcc, s57, v4
	s_nop 1
	v_addc_co_u32_e32 v7, vcc, 0, v5, vcc
	global_load_dword v80, v[6:7], off nt
	v_add_co_u32_e32 v6, vcc, s58, v4
	s_nop 1
	v_addc_co_u32_e32 v7, vcc, 0, v5, vcc
	global_load_dword v81, v[6:7], off nt
	v_add_co_u32_e32 v6, vcc, s59, v4
	s_nop 1
	v_addc_co_u32_e32 v7, vcc, 0, v5, vcc
	v_add_co_u32_e32 v4, vcc, s68, v4
	global_load_dword v82, v[6:7], off nt
	s_nop 0
	v_addc_co_u32_e32 v5, vcc, 0, v5, vcc
	global_load_dword v83, v[4:5], off nt
	s_waitcnt vmcnt(62)
	v_cvt_pk_bf16_f32 v4, v21, v20
	s_waitcnt vmcnt(60)
	v_cvt_pk_bf16_f32 v5, v23, v22
	s_waitcnt vmcnt(58)
	v_cvt_pk_bf16_f32 v6, v25, v24
	s_waitcnt vmcnt(56)
	v_cvt_pk_bf16_f32 v7, v27, v26
	ds_write_b128 v19, v[4:7]
	s_waitcnt vmcnt(54)
	v_cvt_pk_bf16_f32 v4, v29, v28
	s_waitcnt vmcnt(52)
	v_cvt_pk_bf16_f32 v5, v31, v30
	s_waitcnt vmcnt(50)
	v_cvt_pk_bf16_f32 v6, v33, v32
	s_waitcnt vmcnt(48)
	v_cvt_pk_bf16_f32 v7, v35, v34
	ds_write_b128 v19, v[4:7] offset:16
	s_waitcnt vmcnt(46)
	v_cvt_pk_bf16_f32 v4, v37, v36
	s_waitcnt vmcnt(44)
	v_cvt_pk_bf16_f32 v5, v39, v38
	s_waitcnt vmcnt(42)
	v_cvt_pk_bf16_f32 v6, v41, v40
	s_waitcnt vmcnt(40)
	v_cvt_pk_bf16_f32 v7, v43, v42
	ds_write_b128 v19, v[4:7] offset:32
	s_waitcnt vmcnt(38)
	v_cvt_pk_bf16_f32 v4, v45, v44
	s_waitcnt vmcnt(36)
	v_cvt_pk_bf16_f32 v5, v47, v46
	s_waitcnt vmcnt(34)
	v_cvt_pk_bf16_f32 v6, v49, v48
	s_waitcnt vmcnt(32)
	v_cvt_pk_bf16_f32 v7, v51, v50
	ds_write_b128 v19, v[4:7] offset:48
	s_waitcnt vmcnt(30)
	v_cvt_pk_bf16_f32 v4, v53, v52
	s_waitcnt vmcnt(28)
	v_cvt_pk_bf16_f32 v5, v55, v54
	s_waitcnt vmcnt(26)
	v_cvt_pk_bf16_f32 v6, v57, v56
	s_waitcnt vmcnt(24)
	v_cvt_pk_bf16_f32 v7, v59, v58
	ds_write_b128 v19, v[4:7] offset:64
	s_waitcnt vmcnt(22)
	v_cvt_pk_bf16_f32 v4, v61, v60
	s_waitcnt vmcnt(20)
	v_cvt_pk_bf16_f32 v5, v63, v62
	s_waitcnt vmcnt(18)
	v_cvt_pk_bf16_f32 v6, v65, v64
	s_waitcnt vmcnt(16)
	v_cvt_pk_bf16_f32 v7, v67, v66
	ds_write_b128 v19, v[4:7] offset:80
	s_waitcnt vmcnt(14)
	v_cvt_pk_bf16_f32 v4, v69, v68
	s_waitcnt vmcnt(12)
	v_cvt_pk_bf16_f32 v5, v71, v70
	s_waitcnt vmcnt(10)
	v_cvt_pk_bf16_f32 v6, v73, v72
	s_waitcnt vmcnt(8)
	v_cvt_pk_bf16_f32 v7, v75, v74
	ds_write_b128 v19, v[4:7] offset:96
	s_waitcnt vmcnt(6)
	v_cvt_pk_bf16_f32 v4, v77, v76
	s_waitcnt vmcnt(4)
	v_cvt_pk_bf16_f32 v5, v79, v78
	s_waitcnt vmcnt(2)
	v_cvt_pk_bf16_f32 v6, v81, v80
	s_waitcnt vmcnt(0)
	v_cvt_pk_bf16_f32 v7, v83, v82
	ds_write_b128 v19, v[4:7] offset:112
	s_waitcnt lgkmcnt(0)
	v_or_b32_e32 v6, s9, v8
	v_lshl_add_u64 v[4:5], s[10:11], 0, v[2:3]
	v_cmp_gt_i32_e32 vcc, s19, v6
	s_and_saveexec_b64 s[10:11], vcc
	s_cbranch_execz .LBB0_1253
	v_add_u32_e32 v7, v9, v10
	ds_read_b128 v[20:23], v7
	v_ashrrev_i32_e32 v7, 31, v6
	v_lshlrev_b64 v[6:7], 11, v[6:7]
	v_lshl_add_u64 v[6:7], v[4:5], 0, v[6:7]
	s_waitcnt lgkmcnt(0)
	global_store_dwordx4 v[6:7], v[20:23], off nt

.LBB0_1592:
	v_lshl_or_b32 v3, s14, 4, v222
	v_max_i32_e32 v4, 8, v3
	v_add_u32_e32 v4, -8, v4
	v_add_u32_e32 v56, s15, v223
	v_min_u32_e32 v54, 48, v4
	v_sub_u32_e32 v4, v56, v3
	s_lshl_b32 s0, s6, 2
	v_add_u32_e32 v57, 16, v54
	v_max_i32_e32 v4, -15, v4
	s_ashr_i32 s16, s6, 8
	s_bfe_u32 s18, s6, 0x40004
	s_and_b32 s6, s0, 48
	v_cmp_ge_u32_e32 vcc, v56, v54
	v_cmp_lt_u32_e64 s[0:1], v56, v57
	v_add_u32_e32 v4, 15, v4
	v_min_u32_e32 v4, 30, v4
	s_and_b64 vcc, vcc, s[0:1]
	v_cndmask_b32_e32 v227, 31, v4, vcc
	v_or_b32_e32 v4, 1, v56
	v_cmp_ge_u32_e32 vcc, v4, v54
	v_cmp_lt_u32_e64 s[0:1], v4, v57
	v_sub_u32_e32 v4, v4, v3
	v_max_i32_e32 v4, -15, v4
	v_add_u32_e32 v4, 15, v4
	v_min_u32_e32 v4, 30, v4
	s_and_b64 vcc, vcc, s[0:1]
	v_cndmask_b32_e32 v228, 31, v4, vcc
	v_or_b32_e32 v4, 2, v56
	v_cmp_ge_u32_e32 vcc, v4, v54
	v_cmp_lt_u32_e64 s[0:1], v4, v57
	v_sub_u32_e32 v4, v4, v3
	s_ashr_i32 s17, s16, 31
	v_max_i32_e32 v4, -15, v4
	s_add_i32 s20, s6, s91
	s_lshl_b64 s[14:15], s[16:17], 12
	v_add_u32_e32 v58, 15, v4
	v_or_b32_e32 v4, s14, v3
	v_mov_b32_e32 v5, s15
	s_lshl_b32 s14, s20, 6
	s_mov_b32 s15, s7
	s_add_i32 s21, s20, 8
	v_lshl_add_u64 v[204:205], v[4:5], 0, s[14:15]
	s_lshl_b32 s14, s21, 6
	v_sub_u32_e64 v55, s6, 4 clamp
	s_mul_i32 s6, s18, 0x4400
	v_lshl_add_u64 v[206:207], v[4:5], 0, s[14:15]
	s_waitcnt vmcnt(7)
	v_lshl_add_u64 v[22:23], v[204:205], 0, s[6:7]
	v_lshl_add_u64 v[4:5], v[206:207], 0, s[6:7]
	v_lshlrev_b64 v[22:23], 8, v[22:23]
	v_lshlrev_b64 v[4:5], 8, v[4:5]
	s_waitcnt vmcnt(3)
	v_lshl_add_u64 v[38:39], v[194:195], 0, v[22:23]
	v_lshl_add_u64 v[4:5], v[194:195], 0, v[4:5]
	global_load_dwordx4 v[22:25], v[38:39], off
	global_load_dwordx4 v[26:29], v[38:39], off offset:64
	global_load_dwordx4 v[30:33], v[38:39], off offset:128
	global_load_dwordx4 v[34:37], v[38:39], off offset:192
	s_nop 0
	global_load_dwordx4 v[38:41], v[4:5], off
	global_load_dwordx4 v[42:45], v[4:5], off offset:64
	global_load_dwordx4 v[46:49], v[4:5], off offset:128
	global_load_dwordx4 v[50:53], v[4:5], off offset:192
	v_min_u32_e32 v4, 30, v58
	s_and_b64 vcc, vcc, s[0:1]
	v_cndmask_b32_e32 v229, 31, v4, vcc
	v_or_b32_e32 v4, 3, v56
	v_cmp_ge_u32_e32 vcc, v4, v54
	v_cmp_lt_u32_e64 s[0:1], v4, v57
	v_sub_u32_e32 v4, v4, v3
	v_max_i32_e32 v4, -15, v4
	v_add_u32_e32 v4, 15, v4
	v_min_u32_e32 v4, 30, v4
	s_and_b64 vcc, vcc, s[0:1]
	v_cndmask_b32_e32 v230, 31, v4, vcc
	v_or_b32_e32 v4, 4, v56
	v_cmp_ge_u32_e32 vcc, v4, v54
	v_cmp_lt_u32_e64 s[0:1], v4, v57
	v_sub_u32_e32 v4, v4, v3
	v_max_i32_e32 v4, -15, v4
	v_add_u32_e32 v4, 15, v4
	v_min_u32_e32 v4, 30, v4
	s_and_b64 vcc, vcc, s[0:1]
	v_cndmask_b32_e32 v231, 31, v4, vcc
	v_or_b32_e32 v4, 5, v56
	v_cmp_ge_u32_e32 vcc, v4, v54
	v_cmp_lt_u32_e64 s[0:1], v4, v57
	v_sub_u32_e32 v4, v4, v3
	v_max_i32_e32 v4, -15, v4
	v_add_u32_e32 v4, 15, v4
	v_min_u32_e32 v4, 30, v4
	s_and_b64 vcc, vcc, s[0:1]
	v_cndmask_b32_e32 v232, 31, v4, vcc
	v_or_b32_e32 v4, 6, v56
	v_cmp_ge_u32_e32 vcc, v4, v54
	v_cmp_lt_u32_e64 s[0:1], v4, v57
	v_sub_u32_e32 v4, v4, v3
	v_max_i32_e32 v4, -15, v4
	v_add_u32_e32 v4, 15, v4
	v_min_u32_e32 v4, 30, v4
	s_and_b64 vcc, vcc, s[0:1]
	v_cndmask_b32_e32 v233, 31, v4, vcc
	v_or_b32_e32 v4, 7, v56
	v_cmp_ge_u32_e32 vcc, v4, v54
	v_cmp_lt_u32_e64 s[0:1], v4, v57
	v_sub_u32_e32 v3, v4, v3
	s_and_b64 vcc, vcc, s[0:1]
	s_max_i32 s0, s20, 4
	v_max_i32_e32 v3, -15, v3
	s_add_i32 s0, s0, -4
	v_add_u32_e32 v3, 15, v3
	s_min_u32 s22, s0, 56
	s_max_i32 s0, s21, 4
	v_min_u32_e32 v3, 30, v3
	s_add_i32 s0, s0, -4
	v_mov_b32_e32 v4, v2
	v_mov_b32_e32 v5, v2
	v_cndmask_b32_e32 v234, 31, v3, vcc
	s_min_u32 s23, s0, 56
	v_readfirstlane_b32 s0, v55
	v_mov_b32_e32 v3, v2
	v_mov_b64_e32 v[56:57], v[4:5]
	v_mov_b64_e32 v[60:61], v[4:5]
	v_mov_b64_e32 v[64:65], v[4:5]
	v_mov_b64_e32 v[68:69], v[4:5]
	v_mov_b64_e32 v[72:73], v[4:5]
	v_mov_b64_e32 v[76:77], v[4:5]
	v_mov_b64_e32 v[80:81], v[4:5]
	v_mov_b64_e32 v[84:85], v[4:5]
	v_mov_b64_e32 v[88:89], v[4:5]
	v_mov_b64_e32 v[92:93], v[4:5]
	v_mov_b64_e32 v[96:97], v[4:5]
	v_mov_b64_e32 v[100:101], v[4:5]
	v_mov_b64_e32 v[104:105], v[4:5]
	v_mov_b64_e32 v[108:109], v[4:5]
	v_mov_b64_e32 v[112:113], v[4:5]
	v_mov_b64_e32 v[116:117], v[4:5]
	s_min_u32 s24, s0, 41
	v_mov_b32_e32 v235, 0
	v_mov_b32_e32 v236, 0xf149f2ca
	v_mov_b64_e32 v[54:55], v[2:3]
	v_mov_b64_e32 v[58:59], v[2:3]
	v_mov_b64_e32 v[62:63], v[2:3]
	v_mov_b64_e32 v[66:67], v[2:3]
	v_mov_b64_e32 v[70:71], v[2:3]
	v_mov_b64_e32 v[74:75], v[2:3]
	v_mov_b64_e32 v[78:79], v[2:3]
	v_mov_b64_e32 v[82:83], v[2:3]
	v_mov_b64_e32 v[86:87], v[2:3]
	v_mov_b64_e32 v[90:91], v[2:3]
	v_mov_b64_e32 v[94:95], v[2:3]
	v_mov_b64_e32 v[98:99], v[2:3]
	v_mov_b64_e32 v[102:103], v[2:3]
	v_mov_b64_e32 v[106:107], v[2:3]
	v_mov_b64_e32 v[110:111], v[2:3]
	v_mov_b64_e32 v[114:115], v[2:3]
	v_mov_b32_e32 v237, 0xf149f2ca
	v_mov_b32_e32 v3, 0
	s_waitcnt vmcnt(0)
.LBB0_1593:
	s_add_i32 s6, s24, s28
	s_cmp_gt_u32 s28, 22
	s_cselect_b64 s[0:1], -1, 0
	s_cmp_ge_i32 s6, s22
	s_cselect_b64 s[14:15], -1, 0
	s_add_i32 s26, s22, 8
	s_cmp_lt_i32 s6, s26
	s_cselect_b64 s[16:17], -1, 0
	s_and_b64 s[14:15], s[14:15], s[16:17]
	s_or_b64 s[16:17], s[0:1], s[14:15]
	s_cmp_ge_i32 s6, s23
	s_cselect_b64 s[14:15], -1, 0
	s_add_i32 s27, s23, 8
	s_cmp_lt_i32 s6, s27
	s_cselect_b64 s[30:31], -1, 0
	s_and_b64 s[14:15], s[14:15], s[30:31]
	s_or_b64 s[30:31], s[16:17], s[14:15]
	s_andn2_b64 vcc, exec, s[30:31]
	s_cbranch_vccnz .LBB0_1610
	v_add_u32_e32 v4, v225, v226
	ds_read_b128 v[154:157], v224
	ds_read_b128 v[158:161], v224 offset:64
	ds_read_b128 v[174:177], v224 offset:4608
	ds_read_b128 v[162:165], v224 offset:4672
	ds_read_b128 v[166:169], v224 offset:128
	ds_read_b128 v[170:173], v224 offset:192
	ds_read_b128 v[178:181], v224 offset:4736
	ds_read_b128 v[150:153], v224 offset:4800
	ds_read_b128 v[130:133], v4 offset:9216
	ds_read_b128 v[134:137], v4 offset:10752
	ds_read_b128 v[138:141], v4 offset:12288
	ds_read_b128 v[142:145], v4 offset:13824
	ds_read_b128 v[146:149], v4 offset:15360
	ds_read_b128 v[126:129], v4 offset:16896
	ds_read_b128 v[122:125], v4 offset:18432
	ds_read_b128 v[118:121], v4 offset:19968
	s_andn2_b64 vcc, exec, s[16:17]
	s_cbranch_vccnz .LBB0_1602
	s_waitcnt lgkmcnt(14)
	v_mfma_f32_16x16x32_bf16 v[182:185], v[154:157], v[22:25], 0
	s_mov_b64 s[16:17], -1
	s_cmp_lt_u32 s28, 23
	s_waitcnt lgkmcnt(13)
	v_mfma_f32_16x16x32_bf16 v[186:189], v[174:177], v[22:25], 0
	v_mfma_f32_16x16x32_bf16 v[182:185], v[158:161], v[26:29], v[182:185]
	s_waitcnt lgkmcnt(12)
	v_mfma_f32_16x16x32_bf16 v[186:189], v[162:165], v[26:29], v[186:189]
	s_waitcnt lgkmcnt(11)
	v_mfma_f32_16x16x32_bf16 v[182:185], v[166:169], v[30:33], v[182:185]
	s_waitcnt lgkmcnt(9)
	v_mfma_f32_16x16x32_bf16 v[186:189], v[178:181], v[30:33], v[186:189]
	v_mfma_f32_16x16x32_bf16 v[182:185], v[170:173], v[34:37], v[182:185]
	s_waitcnt lgkmcnt(8)
	v_mfma_f32_16x16x32_bf16 v[186:189], v[150:153], v[34:37], v[186:189]
	s_cbranch_scc1 .LBB0_1597
	s_nop 4
	v_pk_mul_f32 v[210:211], v[182:183], s[8:9] op_sel_hi:[1,0]
	v_pk_mul_f32 v[212:213], v[184:185], s[8:9] op_sel_hi:[1,0]
	v_pk_mul_f32 v[4:5], v[186:187], s[8:9] op_sel_hi:[1,0]
	v_pk_mul_f32 v[208:209], v[188:189], s[8:9] op_sel_hi:[1,0]
	s_mov_b64 s[16:17], 0

.LBB0_1602:
	s_or_b64 s[0:1], s[0:1], s[14:15]
	s_andn2_b64 vcc, exec, s[0:1]
	s_cbranch_vccnz .LBB0_1610
	s_waitcnt lgkmcnt(14)
	v_mfma_f32_16x16x32_bf16 v[154:157], v[154:157], v[38:41], 0
	s_mov_b64 s[0:1], -1
	s_cmp_lt_u32 s28, 23
	s_waitcnt lgkmcnt(13)
	v_mfma_f32_16x16x32_bf16 v[174:177], v[174:177], v[38:41], 0
	v_mfma_f32_16x16x32_bf16 v[154:157], v[158:161], v[42:45], v[154:157]
	s_waitcnt lgkmcnt(12)
	v_mfma_f32_16x16x32_bf16 v[158:161], v[162:165], v[42:45], v[174:177]
	s_waitcnt lgkmcnt(11)
	v_mfma_f32_16x16x32_bf16 v[154:157], v[166:169], v[46:49], v[154:157]
	s_waitcnt lgkmcnt(9)
	v_mfma_f32_16x16x32_bf16 v[164:167], v[178:181], v[46:49], v[158:161]
	v_mfma_f32_16x16x32_bf16 v[154:157], v[170:173], v[50:53], v[154:157]
	s_waitcnt lgkmcnt(8)
	v_mfma_f32_16x16x32_bf16 v[150:153], v[150:153], v[50:53], v[164:167]
	s_cbranch_scc1 .LBB0_1605
	s_nop 4
	v_pk_mul_f32 v[160:161], v[154:155], s[8:9] op_sel_hi:[1,0]
	v_pk_mul_f32 v[162:163], v[156:157], s[8:9] op_sel_hi:[1,0]
	v_pk_mul_f32 v[4:5], v[150:151], s[8:9] op_sel_hi:[1,0]
	v_pk_mul_f32 v[158:159], v[152:153], s[8:9] op_sel_hi:[1,0]
	s_mov_b64 s[0:1], 0

.LBB0_1610:
	s_add_i32 s16, s25, 1
	s_cmp_ge_i32 s16, s2
	s_cselect_b64 s[0:1], -1, 0
	s_and_b64 vcc, exec, s[0:1]
	s_cbranch_vccnz .LBB0_1612
	s_add_i32 s98, s25, 2
	s_cmp_ge_i32 s98, s2
	s_cbranch_scc1 .Lnat_st_tail_a
	s_waitcnt vmcnt(3)
	ds_write_b128 v221, v[6:9] offset:21504
	s_waitcnt vmcnt(2)
	ds_write_b128 v220, v[10:13] offset:30720
	s_branch .LBB0_1612
.Lnat_st_tail_a:
	s_waitcnt vmcnt(1)
	ds_write_b128 v221, v[6:9] offset:21504
	s_waitcnt vmcnt(0)
	ds_write_b128 v220, v[10:13] offset:30720

.LBB0_1642:
	v_lshl_or_b32 v3, s14, 4, v222
	v_max_i32_e32 v4, 8, v3
	v_add_u32_e32 v4, -8, v4
	v_add_u32_e32 v56, s15, v223
	v_min_u32_e32 v54, 48, v4
	v_sub_u32_e32 v4, v56, v3
	s_lshl_b32 s0, s6, 2
	v_add_u32_e32 v57, 16, v54
	v_max_i32_e32 v4, -15, v4
	s_ashr_i32 s16, s6, 8
	s_bfe_u32 s18, s6, 0x40004
	s_and_b32 s6, s0, 48
	v_cmp_ge_u32_e32 vcc, v56, v54
	v_cmp_lt_u32_e64 s[0:1], v56, v57
	v_add_u32_e32 v4, 15, v4
	v_min_u32_e32 v4, 30, v4
	s_and_b64 vcc, vcc, s[0:1]
	v_cndmask_b32_e32 v227, 31, v4, vcc
	v_or_b32_e32 v4, 1, v56
	v_cmp_ge_u32_e32 vcc, v4, v54
	v_cmp_lt_u32_e64 s[0:1], v4, v57
	v_sub_u32_e32 v4, v4, v3
	v_max_i32_e32 v4, -15, v4
	v_add_u32_e32 v4, 15, v4
	v_min_u32_e32 v4, 30, v4
	s_and_b64 vcc, vcc, s[0:1]
	v_cndmask_b32_e32 v228, 31, v4, vcc
	v_or_b32_e32 v4, 2, v56
	v_cmp_ge_u32_e32 vcc, v4, v54
	v_cmp_lt_u32_e64 s[0:1], v4, v57
	v_sub_u32_e32 v4, v4, v3
	v_max_i32_e32 v4, -15, v4
	s_ashr_i32 s17, s16, 31
	v_add_u32_e32 v4, 15, v4
	s_add_i32 s20, s6, s91
	s_lshl_b64 s[14:15], s[16:17], 12
	v_min_u32_e32 v58, 30, v4
	v_or_b32_e32 v4, s14, v3
	v_mov_b32_e32 v5, s15
	s_lshl_b32 s14, s20, 6
	s_mov_b32 s15, s7
	s_add_i32 s21, s20, 8
	v_lshl_add_u64 v[204:205], v[4:5], 0, s[14:15]
	s_lshl_b32 s14, s21, 6
	v_sub_u32_e64 v55, s6, 4 clamp
	s_mul_i32 s6, s18, 0x4400
	v_lshl_add_u64 v[206:207], v[4:5], 0, s[14:15]
	s_waitcnt vmcnt(7)
	v_lshl_add_u64 v[22:23], v[204:205], 0, s[6:7]
	v_lshl_add_u64 v[4:5], v[206:207], 0, s[6:7]
	v_lshlrev_b64 v[22:23], 8, v[22:23]
	v_lshlrev_b64 v[4:5], 8, v[4:5]
	s_waitcnt vmcnt(3)
	v_lshl_add_u64 v[38:39], v[194:195], 0, v[22:23]
	v_lshl_add_u64 v[4:5], v[194:195], 0, v[4:5]
	global_load_dwordx4 v[22:25], v[38:39], off
	global_load_dwordx4 v[26:29], v[38:39], off offset:64
	global_load_dwordx4 v[30:33], v[38:39], off offset:128
	global_load_dwordx4 v[34:37], v[38:39], off offset:192
	s_nop 0
	global_load_dwordx4 v[38:41], v[4:5], off
	global_load_dwordx4 v[42:45], v[4:5], off offset:64
	global_load_dwordx4 v[46:49], v[4:5], off offset:128
	global_load_dwordx4 v[50:53], v[4:5], off offset:192
	s_and_b64 vcc, vcc, s[0:1]
	v_or_b32_e32 v4, 3, v56
	v_cndmask_b32_e32 v229, 31, v58, vcc
	v_cmp_ge_u32_e32 vcc, v4, v54
	v_cmp_lt_u32_e64 s[0:1], v4, v57
	v_sub_u32_e32 v4, v4, v3
	v_max_i32_e32 v4, -15, v4
	v_add_u32_e32 v4, 15, v4
	v_min_u32_e32 v4, 30, v4
	s_and_b64 vcc, vcc, s[0:1]
	v_cndmask_b32_e32 v230, 31, v4, vcc
	v_or_b32_e32 v4, 4, v56
	v_cmp_ge_u32_e32 vcc, v4, v54
	v_cmp_lt_u32_e64 s[0:1], v4, v57
	v_sub_u32_e32 v4, v4, v3
	v_max_i32_e32 v4, -15, v4
	v_add_u32_e32 v4, 15, v4
	v_min_u32_e32 v4, 30, v4
	s_and_b64 vcc, vcc, s[0:1]
	v_cndmask_b32_e32 v231, 31, v4, vcc
	v_or_b32_e32 v4, 5, v56
	v_cmp_ge_u32_e32 vcc, v4, v54
	v_cmp_lt_u32_e64 s[0:1], v4, v57
	v_sub_u32_e32 v4, v4, v3
	v_max_i32_e32 v4, -15, v4
	v_add_u32_e32 v4, 15, v4
	v_min_u32_e32 v4, 30, v4
	s_and_b64 vcc, vcc, s[0:1]
	v_cndmask_b32_e32 v232, 31, v4, vcc
	v_or_b32_e32 v4, 6, v56
	v_cmp_ge_u32_e32 vcc, v4, v54
	v_cmp_lt_u32_e64 s[0:1], v4, v57
	v_sub_u32_e32 v4, v4, v3
	v_max_i32_e32 v4, -15, v4
	v_add_u32_e32 v4, 15, v4
	v_min_u32_e32 v4, 30, v4
	s_and_b64 vcc, vcc, s[0:1]
	v_cndmask_b32_e32 v233, 31, v4, vcc
	v_or_b32_e32 v4, 7, v56
	v_cmp_ge_u32_e32 vcc, v4, v54
	v_cmp_lt_u32_e64 s[0:1], v4, v57
	v_sub_u32_e32 v3, v4, v3
	s_and_b64 vcc, vcc, s[0:1]
	s_max_i32 s0, s20, 4
	v_max_i32_e32 v3, -15, v3
	s_add_i32 s0, s0, -4
	v_add_u32_e32 v3, 15, v3
	s_min_u32 s22, s0, 56
	s_max_i32 s0, s21, 4
	v_min_u32_e32 v3, 30, v3
	s_add_i32 s0, s0, -4
	v_mov_b32_e32 v4, v2
	v_mov_b32_e32 v5, v2
	v_cndmask_b32_e32 v234, 31, v3, vcc
	s_min_u32 s23, s0, 56
	v_readfirstlane_b32 s0, v55
	v_mov_b32_e32 v3, v2
	v_mov_b64_e32 v[56:57], v[4:5]
	v_mov_b64_e32 v[60:61], v[4:5]
	v_mov_b64_e32 v[64:65], v[4:5]
	v_mov_b64_e32 v[68:69], v[4:5]
	v_mov_b64_e32 v[72:73], v[4:5]
	v_mov_b64_e32 v[76:77], v[4:5]
	v_mov_b64_e32 v[80:81], v[4:5]
	v_mov_b64_e32 v[84:85], v[4:5]
	v_mov_b64_e32 v[88:89], v[4:5]
	v_mov_b64_e32 v[92:93], v[4:5]
	v_mov_b64_e32 v[96:97], v[4:5]
	v_mov_b64_e32 v[100:101], v[4:5]
	v_mov_b64_e32 v[104:105], v[4:5]
	v_mov_b64_e32 v[108:109], v[4:5]
	v_mov_b64_e32 v[112:113], v[4:5]
	v_mov_b64_e32 v[116:117], v[4:5]
	s_min_u32 s24, s0, 41
	s_add_i32 s26, s22, 8
	s_add_i32 s27, s23, 8
	v_mov_b32_e32 v235, 0
	v_mov_b32_e32 v236, 0xf149f2ca
	v_mov_b64_e32 v[54:55], v[2:3]
	v_mov_b64_e32 v[58:59], v[2:3]
	v_mov_b64_e32 v[62:63], v[2:3]
	v_mov_b64_e32 v[66:67], v[2:3]
	v_mov_b64_e32 v[70:71], v[2:3]
	v_mov_b64_e32 v[74:75], v[2:3]
	v_mov_b64_e32 v[78:79], v[2:3]
	v_mov_b64_e32 v[82:83], v[2:3]
	v_mov_b64_e32 v[86:87], v[2:3]
	v_mov_b64_e32 v[90:91], v[2:3]
	v_mov_b64_e32 v[94:95], v[2:3]
	v_mov_b64_e32 v[98:99], v[2:3]
	v_mov_b64_e32 v[102:103], v[2:3]
	v_mov_b64_e32 v[106:107], v[2:3]
	v_mov_b64_e32 v[110:111], v[2:3]
	v_mov_b64_e32 v[114:115], v[2:3]
	v_mov_b32_e32 v237, 0xf149f2ca
	v_mov_b32_e32 v3, 0
	s_waitcnt vmcnt(0)
.LBB0_1643:
	s_add_i32 s6, s24, s28
	s_cmp_gt_u32 s28, 22
	s_cselect_b64 s[0:1], -1, 0
	s_cmp_ge_i32 s6, s22
	s_cselect_b64 s[14:15], -1, 0
	s_cmp_lt_i32 s6, s26
	s_cselect_b64 s[16:17], -1, 0
	s_and_b64 s[14:15], s[14:15], s[16:17]
	s_or_b64 s[16:17], s[0:1], s[14:15]
	s_cmp_ge_i32 s6, s23
	s_cselect_b64 s[14:15], -1, 0
	s_cmp_lt_i32 s6, s27
	s_cselect_b64 s[26:27], -1, 0
	s_and_b64 s[14:15], s[14:15], s[26:27]
	s_or_b64 s[26:27], s[16:17], s[14:15]
	s_andn2_b64 vcc, exec, s[26:27]
	s_cbranch_vccnz .LBB0_1660
	v_add_u32_e32 v4, v225, v226
	ds_read_b128 v[154:157], v224 offset:21504
	ds_read_b128 v[158:161], v224 offset:21568
	ds_read_b128 v[174:177], v224 offset:26112
	ds_read_b128 v[162:165], v224 offset:26176
	ds_read_b128 v[166:169], v224 offset:21632
	ds_read_b128 v[170:173], v224 offset:21696
	ds_read_b128 v[178:181], v224 offset:26240
	ds_read_b128 v[150:153], v224 offset:26304
	ds_read_b128 v[130:133], v4 offset:30720
	ds_read_b128 v[134:137], v4 offset:32256
	ds_read_b128 v[138:141], v4 offset:33792
	ds_read_b128 v[142:145], v4 offset:35328
	ds_read_b128 v[146:149], v4 offset:36864
	ds_read_b128 v[126:129], v4 offset:38400
	ds_read_b128 v[122:125], v4 offset:39936
	ds_read_b128 v[118:121], v4 offset:41472
	s_andn2_b64 vcc, exec, s[16:17]
	s_cbranch_vccnz .LBB0_1652
	s_waitcnt lgkmcnt(14)
	v_mfma_f32_16x16x32_bf16 v[182:185], v[154:157], v[22:25], 0
	s_mov_b64 s[16:17], -1
	s_cmp_lt_u32 s28, 23
	s_waitcnt lgkmcnt(13)
	v_mfma_f32_16x16x32_bf16 v[186:189], v[174:177], v[22:25], 0
	v_mfma_f32_16x16x32_bf16 v[182:185], v[158:161], v[26:29], v[182:185]
	s_waitcnt lgkmcnt(12)
	v_mfma_f32_16x16x32_bf16 v[186:189], v[162:165], v[26:29], v[186:189]
	s_waitcnt lgkmcnt(11)
	v_mfma_f32_16x16x32_bf16 v[182:185], v[166:169], v[30:33], v[182:185]
	s_waitcnt lgkmcnt(9)
	v_mfma_f32_16x16x32_bf16 v[186:189], v[178:181], v[30:33], v[186:189]
	v_mfma_f32_16x16x32_bf16 v[182:185], v[170:173], v[34:37], v[182:185]
	s_waitcnt lgkmcnt(8)
	v_mfma_f32_16x16x32_bf16 v[186:189], v[150:153], v[34:37], v[186:189]
	s_cbranch_scc1 .LBB0_1647
	s_nop 4
	v_pk_mul_f32 v[4:5], v[182:183], s[8:9] op_sel_hi:[1,0]
	v_pk_mul_f32 v[210:211], v[184:185], s[8:9] op_sel_hi:[1,0]
	v_pk_mul_f32 v[208:209], v[186:187], s[8:9] op_sel_hi:[1,0]
	v_pk_mul_f32 v[212:213], v[188:189], s[8:9] op_sel_hi:[1,0]
	s_mov_b64 s[16:17], 0

.LBB0_1652:
	s_or_b64 s[0:1], s[0:1], s[14:15]
	s_andn2_b64 vcc, exec, s[0:1]
	s_cbranch_vccnz .LBB0_1660
	s_waitcnt lgkmcnt(14)
	v_mfma_f32_16x16x32_bf16 v[154:157], v[154:157], v[38:41], 0
	s_mov_b64 s[0:1], -1
	s_cmp_lt_u32 s28, 23
	s_waitcnt lgkmcnt(13)
	v_mfma_f32_16x16x32_bf16 v[174:177], v[174:177], v[38:41], 0
	v_mfma_f32_16x16x32_bf16 v[154:157], v[158:161], v[42:45], v[154:157]
	s_waitcnt lgkmcnt(12)
	v_mfma_f32_16x16x32_bf16 v[158:161], v[162:165], v[42:45], v[174:177]
	s_waitcnt lgkmcnt(11)
	v_mfma_f32_16x16x32_bf16 v[154:157], v[166:169], v[46:49], v[154:157]
	s_waitcnt lgkmcnt(9)
	v_mfma_f32_16x16x32_bf16 v[164:167], v[178:181], v[46:49], v[158:161]
	v_mfma_f32_16x16x32_bf16 v[154:157], v[170:173], v[50:53], v[154:157]
	s_waitcnt lgkmcnt(8)
	v_mfma_f32_16x16x32_bf16 v[150:153], v[150:153], v[50:53], v[164:167]
	s_cbranch_scc1 .LBB0_1655
	s_nop 4
	v_pk_mul_f32 v[4:5], v[154:155], s[8:9] op_sel_hi:[1,0]
	v_pk_mul_f32 v[160:161], v[156:157], s[8:9] op_sel_hi:[1,0]
	v_pk_mul_f32 v[158:159], v[150:151], s[8:9] op_sel_hi:[1,0]
	v_pk_mul_f32 v[162:163], v[152:153], s[8:9] op_sel_hi:[1,0]
	s_mov_b64 s[0:1], 0

.LBB0_1660:
	s_add_i32 s14, s25, 2
	s_cmp_ge_i32 s14, s2
	s_cbranch_scc1 .LBB0_1662
	s_add_i32 s98, s25, 3
	s_cmp_ge_i32 s98, s2
	s_cbranch_scc1 .Lnat_st_tail_b
	s_waitcnt vmcnt(3)
	ds_write_b128 v221, v[14:17]
	s_waitcnt vmcnt(2)
	ds_write_b128 v220, v[18:21] offset:9216
	s_branch .LBB0_1662
.Lnat_st_tail_b:
	s_waitcnt vmcnt(1)
	ds_write_b128 v221, v[14:17]
	s_waitcnt vmcnt(0)
	ds_write_b128 v220, v[18:21] offset:9216

.LBB0_1999:
	s_or_b64 exec, exec, s[4:5]
	s_nop 0
	v_add_u32_e32 v114, v164, v170
	v_cmp_lt_i32_e32 vcc, v114, v139
	s_and_saveexec_b64 s[4:5], vcc
	s_cbranch_execz .LBB0_2001
	s_nop 0
	v_ashrrev_i32_e32 v159, 31, v158
	v_lshlrev_b64 v[114:115], 12, v[158:159]
	v_lshl_add_u64 v[114:115], s[18:19], 0, v[114:115]
	v_lshl_add_u64 v[114:115], v[146:147], 1, v[114:115]
	v_pk_mul_f32 v[112:113], v[112:113], v[142:143] op_sel_hi:[1,0]
	v_pk_mul_f32 v[110:111], v[110:111], v[142:143] op_sel_hi:[1,0]
	v_pk_mul_f32 v[116:117], v[108:109], v[142:143] op_sel_hi:[1,0]
	v_pk_mul_f32 v[108:109], v[106:107], v[142:143] op_sel_hi:[1,0]
	v_cvt_pk_bf16_f32 v106, v110, v111
	v_cvt_pk_bf16_f32 v107, v112, v113
	v_pk_mul_f32 v[104:105], v[104:105], v[142:143] op_sel_hi:[1,0]
	v_cvt_pk_bf16_f32 v108, v108, v109
	v_cvt_pk_bf16_f32 v109, v116, v117
	global_store_dwordx4 v[114:115], v[106:109], off
	v_pk_mul_f32 v[102:103], v[102:103], v[142:143] op_sel_hi:[1,0]
	s_nop 0
	v_pk_mul_f32 v[106:107], v[100:101], v[142:143] op_sel_hi:[1,0]
	v_pk_mul_f32 v[100:101], v[98:99], v[142:143] op_sel_hi:[1,0]
	v_cvt_pk_bf16_f32 v98, v102, v103
	v_cvt_pk_bf16_f32 v99, v104, v105
	s_nop 0
	v_cvt_pk_bf16_f32 v100, v100, v101
	v_cvt_pk_bf16_f32 v101, v106, v107
	global_store_dwordx4 v[114:115], v[98:101], off offset:256
.LBB0_2001:
	s_or_b64 exec, exec, s[4:5]
	s_nop 0
	v_add_u32_e32 v98, v165, v170
	v_cmp_lt_i32_e32 vcc, v98, v139
	s_and_saveexec_b64 s[4:5], vcc
	s_cbranch_execz .LBB0_2003
	s_nop 0
	v_ashrrev_i32_e32 v157, 31, v156
	v_lshlrev_b64 v[98:99], 12, v[156:157]
	v_lshl_add_u64 v[98:99], s[18:19], 0, v[98:99]
	v_lshl_add_u64 v[98:99], v[146:147], 1, v[98:99]
	v_pk_mul_f32 v[96:97], v[96:97], v[138:139] op_sel_hi:[1,0]
	v_pk_mul_f32 v[94:95], v[94:95], v[138:139] op_sel_hi:[1,0]
	v_pk_mul_f32 v[100:101], v[92:93], v[138:139] op_sel_hi:[1,0]
	v_pk_mul_f32 v[92:93], v[90:91], v[138:139] op_sel_hi:[1,0]
	v_cvt_pk_bf16_f32 v90, v94, v95
	v_cvt_pk_bf16_f32 v91, v96, v97
	v_pk_mul_f32 v[88:89], v[88:89], v[138:139] op_sel_hi:[1,0]
	v_cvt_pk_bf16_f32 v92, v92, v93
	v_cvt_pk_bf16_f32 v93, v100, v101
	global_store_dwordx4 v[98:99], v[90:93], off
	v_pk_mul_f32 v[86:87], v[86:87], v[138:139] op_sel_hi:[1,0]
	s_nop 0
	v_pk_mul_f32 v[90:91], v[84:85], v[138:139] op_sel_hi:[1,0]
	v_pk_mul_f32 v[84:85], v[82:83], v[138:139] op_sel_hi:[1,0]
	v_cvt_pk_bf16_f32 v82, v86, v87
	v_cvt_pk_bf16_f32 v83, v88, v89
	s_nop 0
	v_cvt_pk_bf16_f32 v84, v84, v85
	v_cvt_pk_bf16_f32 v85, v90, v91
	global_store_dwordx4 v[98:99], v[82:85], off offset:256
.LBB0_2003:
	s_or_b64 exec, exec, s[4:5]
	s_nop 0
	v_add_u32_e32 v82, v166, v170
	v_cmp_lt_i32_e32 vcc, v82, v139
	s_and_saveexec_b64 s[4:5], vcc
	s_cbranch_execz .LBB0_2005
	s_nop 0
	v_ashrrev_i32_e32 v155, 31, v154
	v_lshlrev_b64 v[82:83], 12, v[154:155]
	v_lshl_add_u64 v[82:83], s[18:19], 0, v[82:83]
	v_lshl_add_u64 v[82:83], v[146:147], 1, v[82:83]
	v_pk_mul_f32 v[80:81], v[80:81], v[136:137] op_sel_hi:[1,0]
	v_pk_mul_f32 v[78:79], v[78:79], v[136:137] op_sel_hi:[1,0]
	v_pk_mul_f32 v[84:85], v[76:77], v[136:137] op_sel_hi:[1,0]
	v_pk_mul_f32 v[76:77], v[74:75], v[136:137] op_sel_hi:[1,0]
	v_cvt_pk_bf16_f32 v74, v78, v79
	v_cvt_pk_bf16_f32 v75, v80, v81
	v_pk_mul_f32 v[72:73], v[72:73], v[136:137] op_sel_hi:[1,0]
	v_cvt_pk_bf16_f32 v76, v76, v77
	v_cvt_pk_bf16_f32 v77, v84, v85
	global_store_dwordx4 v[82:83], v[74:77], off
	v_pk_mul_f32 v[70:71], v[70:71], v[136:137] op_sel_hi:[1,0]
	s_nop 0
	v_pk_mul_f32 v[74:75], v[68:69], v[136:137] op_sel_hi:[1,0]
	v_pk_mul_f32 v[68:69], v[66:67], v[136:137] op_sel_hi:[1,0]
	v_cvt_pk_bf16_f32 v66, v70, v71
	v_cvt_pk_bf16_f32 v67, v72, v73
	s_nop 0
	v_cvt_pk_bf16_f32 v68, v68, v69
	v_cvt_pk_bf16_f32 v69, v74, v75
	global_store_dwordx4 v[82:83], v[66:69], off offset:256

.LBB0_2008:
	s_nop 0
	v_ashrrev_i32_e32 v73, 31, v72
	v_lshlrev_b64 v[26:27], 12, v[72:73]
	v_lshl_add_u64 v[26:27], s[18:19], 0, v[26:27]
	v_pk_mul_f32 v[28:29], v[12:13], v[70:71] op_sel_hi:[1,0]
	v_pk_mul_f32 v[12:13], v[10:11], v[70:71] op_sel_hi:[1,0]
	v_lshl_add_u64 v[26:27], v[146:147], 1, v[26:27]
	v_pk_mul_f32 v[16:17], v[16:17], v[70:71] op_sel_hi:[1,0]
	v_pk_mul_f32 v[14:15], v[14:15], v[70:71] op_sel_hi:[1,0]
	s_nop 0
	v_cvt_pk_bf16_f32 v10, v14, v15
	v_cvt_pk_bf16_f32 v11, v16, v17
	v_cvt_pk_bf16_f32 v12, v12, v13
	v_cvt_pk_bf16_f32 v13, v28, v29
	global_store_dwordx4 v[26:27], v[10:13], off
	v_pk_mul_f32 v[14:15], v[40:41], v[70:71] op_sel_hi:[1,0]
	v_pk_mul_f32 v[16:17], v[38:39], v[70:71] op_sel_hi:[1,0]
	v_pk_mul_f32 v[12:13], v[36:37], v[70:71] op_sel_hi:[1,0]
	v_pk_mul_f32 v[10:11], v[34:35], v[70:71] op_sel_hi:[1,0]
	s_nop 0
	v_cvt_pk_bf16_f32 v10, v10, v11
	v_cvt_pk_bf16_f32 v11, v12, v13
	v_cvt_pk_bf16_f32 v12, v16, v17
	v_cvt_pk_bf16_f32 v13, v14, v15
	global_store_dwordx4 v[26:27], v[10:13], off offset:256
	s_or_b64 exec, exec, s[4:5]
	v_cmp_lt_i32_e32 vcc, v67, v139
	s_and_saveexec_b64 s[4:5], vcc
	s_cbranch_execnz .LBB0_2013

.LBB0_2011:
	s_nop 0
	v_ashrrev_i32_e32 v77, 31, v76
	v_lshlrev_b64 v[50:51], 12, v[76:77]
	v_lshl_add_u64 v[50:51], s[18:19], 0, v[50:51]
	v_lshl_add_u64 v[50:51], v[146:147], 1, v[50:51]
	v_pk_mul_f32 v[48:49], v[48:49], v[74:75] op_sel_hi:[1,0]
	v_pk_mul_f32 v[46:47], v[46:47], v[74:75] op_sel_hi:[1,0]
	v_pk_mul_f32 v[52:53], v[44:45], v[74:75] op_sel_hi:[1,0]
	v_pk_mul_f32 v[44:45], v[42:43], v[74:75] op_sel_hi:[1,0]
	v_cvt_pk_bf16_f32 v42, v46, v47
	v_cvt_pk_bf16_f32 v43, v48, v49
	v_pk_mul_f32 v[32:33], v[32:33], v[74:75] op_sel_hi:[1,0]
	v_cvt_pk_bf16_f32 v44, v44, v45
	v_cvt_pk_bf16_f32 v45, v52, v53
	global_store_dwordx4 v[50:51], v[42:45], off
	v_pk_mul_f32 v[30:31], v[30:31], v[74:75] op_sel_hi:[1,0]
	s_nop 0
	v_pk_mul_f32 v[42:43], v[28:29], v[74:75] op_sel_hi:[1,0]
	v_pk_mul_f32 v[28:29], v[26:27], v[74:75] op_sel_hi:[1,0]
	v_cvt_pk_bf16_f32 v26, v30, v31
	v_cvt_pk_bf16_f32 v27, v32, v33
	s_nop 0
	v_cvt_pk_bf16_f32 v28, v28, v29
	v_cvt_pk_bf16_f32 v29, v42, v43
	global_store_dwordx4 v[50:51], v[26:29], off offset:256
	s_or_b64 exec, exec, s[4:5]
	v_cmp_lt_i32_e32 vcc, v69, v139
	s_and_saveexec_b64 s[4:5], vcc
	s_cbranch_execnz .LBB0_2008

.LBB0_2013:
	s_nop 0
	v_ashrrev_i32_e32 v69, 31, v68
	v_lshlrev_b64 v[10:11], 12, v[68:69]
	v_lshl_add_u64 v[10:11], s[18:19], 0, v[10:11]
	v_pk_mul_f32 v[12:13], v[4:5], v[66:67] op_sel_hi:[1,0]
	v_pk_mul_f32 v[4:5], v[2:3], v[66:67] op_sel_hi:[1,0]
	v_lshl_add_u64 v[10:11], v[146:147], 1, v[10:11]
	v_pk_mul_f32 v[8:9], v[8:9], v[66:67] op_sel_hi:[1,0]
	v_pk_mul_f32 v[6:7], v[6:7], v[66:67] op_sel_hi:[1,0]
	s_nop 0
	v_cvt_pk_bf16_f32 v2, v6, v7
	v_cvt_pk_bf16_f32 v3, v8, v9
	v_cvt_pk_bf16_f32 v4, v4, v5
	v_cvt_pk_bf16_f32 v5, v12, v13
	global_store_dwordx4 v[10:11], v[2:5], off
	v_pk_mul_f32 v[6:7], v[24:25], v[66:67] op_sel_hi:[1,0]
	v_pk_mul_f32 v[8:9], v[22:23], v[66:67] op_sel_hi:[1,0]
	v_pk_mul_f32 v[4:5], v[20:21], v[66:67] op_sel_hi:[1,0]
	v_pk_mul_f32 v[2:3], v[18:19], v[66:67] op_sel_hi:[1,0]
	s_nop 0
	v_cvt_pk_bf16_f32 v2, v2, v3
	v_cvt_pk_bf16_f32 v3, v4, v5
	v_cvt_pk_bf16_f32 v4, v8, v9
	v_cvt_pk_bf16_f32 v5, v6, v7
	global_store_dwordx4 v[10:11], v[2:5], off offset:256
	s_or_b64 exec, exec, s[4:5]
	s_and_b64 vcc, exec, s[0:1]
	s_mov_b64 s[0:1], -1
	s_cbranch_vccnz .LBB0_1988

	.amdhsa_kernel _Z6mk_fwd4Args
		.amdhsa_group_segment_fixed_size 0
		.amdhsa_private_segment_fixed_size 0
		.amdhsa_kernarg_size 464
		.amdhsa_user_sgpr_count 2
		.amdhsa_user_sgpr_dispatch_ptr 0
		.amdhsa_user_sgpr_queue_ptr 0
		.amdhsa_user_sgpr_kernarg_segment_ptr 1
		.amdhsa_user_sgpr_dispatch_id 0
		.amdhsa_user_sgpr_kernarg_preload_length 0
		.amdhsa_user_sgpr_kernarg_preload_offset 0
		.amdhsa_user_sgpr_private_segment_size 0
		.amdhsa_uses_dynamic_stack 0
		.amdhsa_enable_private_segment 0
		.amdhsa_system_sgpr_workgroup_id_x 1
		.amdhsa_system_sgpr_workgroup_id_y 0
		.amdhsa_system_sgpr_workgroup_id_z 0
		.amdhsa_system_sgpr_workgroup_info 0
		.amdhsa_system_vgpr_workitem_id 0
		.amdhsa_next_free_vgpr 256
		.amdhsa_next_free_sgpr 100
		.amdhsa_accum_offset 256
		.amdhsa_reserve_vcc 1
		.amdhsa_float_round_mode_32 0
		.amdhsa_float_round_mode_16_64 0
		.amdhsa_float_denorm_mode_32 3
		.amdhsa_float_denorm_mode_16_64 3
		.amdhsa_dx10_clamp 1
		.amdhsa_ieee_mode 1
		.amdhsa_fp16_overflow 0
		.amdhsa_tg_split 0
		.amdhsa_exception_fp_ieee_invalid_op 0
		.amdhsa_exception_fp_denorm_src 0
		.amdhsa_exception_fp_ieee_div_zero 0
		.amdhsa_exception_fp_ieee_overflow 0
		.amdhsa_exception_fp_ieee_underflow 0
		.amdhsa_exception_fp_ieee_inexact 0
		.amdhsa_exception_int_div_zero 0
	.end_amdhsa_kernel

amdhsa.kernels:
  - .agpr_count:     0
    .args:
      - .offset:         0
        .size:           208
        .value_kind:     by_value
      - .offset:         208
        .size:           4
        .value_kind:     hidden_block_count_x
      - .offset:         212
        .size:           4
        .value_kind:     hidden_block_count_y
      - .offset:         216
        .size:           4
        .value_kind:     hidden_block_count_z
      - .offset:         220
        .size:           2
        .value_kind:     hidden_group_size_x
      - .offset:         222
        .size:           2
        .value_kind:     hidden_group_size_y
      - .offset:         224
        .size:           2
        .value_kind:     hidden_group_size_z
      - .offset:         226
        .size:           2
        .value_kind:     hidden_remainder_x
      - .offset:         228
        .size:           2
        .value_kind:     hidden_remainder_y
      - .offset:         230
        .size:           2
        .value_kind:     hidden_remainder_z
      - .offset:         248
        .size:           8
        .value_kind:     hidden_global_offset_x
      - .offset:         256
        .size:           8
        .value_kind:     hidden_global_offset_y
      - .offset:         264
        .size:           8
        .value_kind:     hidden_global_offset_z
      - .offset:         272
        .size:           2
        .value_kind:     hidden_grid_dims
      - .offset:         328
        .size:           4
        .value_kind:     hidden_dynamic_lds_size
    .group_segment_fixed_size: 0
    .kernarg_segment_align: 8
    .kernarg_segment_size: 464
    .language:       OpenCL C
    .language_version:
      - 2
      - 0
    .max_flat_workgroup_size: 512
    .name:           _Z6mk_fwd4Args
    .private_segment_fixed_size: 0
    .sgpr_count:     106
    .sgpr_spill_count: 66
    .symbol:         _Z6mk_fwd4Args.kd
    .uniform_work_group_size: 1
    .uses_dynamic_stack: false
    .vgpr_count:     256
    .vgpr_spill_count: 0
    .wavefront_size: 64
